# baseline (speedup 1.0000x reference)
.LBB0_484:
	s_add_i32 s57, s57, 1
	v_cvt_f32_ubyte0_e32 v0, s57
	v_mul_f32_e32 v1, -0.5, v0
	s_mov_b32 s56, 0xc2fc0000
	v_cmp_gt_f32_e32 vcc, s56, v1
	s_and_b64 s[58:59], vcc, exec
	s_cselect_b32 s57, 0xffffffc0, 0
	v_cndmask_b32_e32 v1, 0, v191, vcc
	v_fmac_f32_e32 v1, -0.5, v0
	v_exp_f32_e32 v0, v1
	v_cmp_nlg_f32_e32 vcc, s23, v17
	s_or_b64 vcc, s[0:1], vcc
	v_mov_b32_e32 v14, v117
	v_cndmask_b32_e32 v1, v17, v192, vcc
	v_cmp_gt_f32_e64 s[0:1], v16, v1
	v_ldexp_f32 v0, v0, s57
	s_and_b64 s[0:1], s[6:7], s[0:1]
	v_mul_f32_e32 v137, 0x3fb8aa3b, v0
	v_cndmask_b32_e64 v0, 0, -1, vcc
	v_cndmask_b32_e64 v1, v1, v16, s[0:1]
	v_cndmask_b32_e64 v0, v0, 1, s[0:1]
	v_cmp_gt_f32_e64 s[0:1], v35, v1
	s_and_b64 s[0:1], s[44:45], s[0:1]
	s_lshl_b32 s57, s30, 2
	v_cndmask_b32_e64 v1, v1, v35, s[0:1]
	v_cndmask_b32_e64 v0, v0, 2, s[0:1]
	v_cmp_gt_f32_e64 s[0:1], v34, v1
	s_and_b64 s[0:1], s[46:47], s[0:1]
	s_add_i32 s57, s57, 4
	v_cndmask_b32_e64 v1, v1, v34, s[0:1]
	v_cndmask_b32_e64 v0, v0, 3, s[0:1]
	v_cmp_gt_f32_e64 s[0:1], v37, v1
	s_and_b64 s[0:1], s[48:49], s[0:1]
	v_mov_b32_e32 v15, v117
	v_cndmask_b32_e64 v1, v1, v37, s[0:1]
	v_cndmask_b32_e64 v0, v0, 4, s[0:1]
	v_cmp_gt_f32_e64 s[0:1], v36, v1
	s_and_b64 s[0:1], s[50:51], s[0:1]
	v_mul_f32_e32 v138, 0x42000000, v137
	v_cndmask_b32_e64 v1, v1, v36, s[0:1]
	v_cndmask_b32_e64 v0, v0, 5, s[0:1]
	v_cmp_gt_f32_e64 s[0:1], v38, v1
	s_and_b64 s[0:1], s[52:53], s[0:1]
	v_mov_b32_e32 v6, v117
	v_cndmask_b32_e64 v0, v0, 6, s[0:1]
	v_lshlrev_b32_e64 v1, v0, 1
	v_cmp_lt_i32_e64 s[0:1], -1, v0
	v_mov_b32_e32 v7, v117
	v_mov_b32_e32 v8, v117
	v_cndmask_b32_e64 v0, 0, v1, s[0:1]
	v_and_b32_e32 v1, 1, v0
	v_cmp_eq_u32_e64 s[0:1], 1, v1
	s_or_b64 s[0:1], vcc, s[0:1]
	v_and_b32_e32 v3, 2, v0
	v_cndmask_b32_e64 v1, 0, -1, s[0:1]
	v_cndmask_b32_e64 v2, v17, v192, s[0:1]
	v_cmp_eq_u32_e64 s[0:1], 0, v3
	s_and_b64 s[58:59], s[6:7], s[0:1]
	v_cmp_gt_f32_e64 s[0:1], v16, v2
	s_and_b64 s[0:1], s[58:59], s[0:1]
	v_and_b32_e32 v3, 4, v0
	v_cndmask_b32_e64 v1, v1, 1, s[0:1]
	v_cndmask_b32_e64 v2, v2, v16, s[0:1]
	v_cmp_eq_u32_e64 s[0:1], 0, v3
	s_and_b64 s[58:59], s[44:45], s[0:1]
	v_cmp_gt_f32_e64 s[0:1], v35, v2
	s_and_b64 s[0:1], s[58:59], s[0:1]
	v_and_b32_e32 v3, 8, v0
	v_cndmask_b32_e64 v1, v1, 2, s[0:1]
	v_cndmask_b32_e64 v2, v2, v35, s[0:1]
	v_cmp_eq_u32_e64 s[0:1], 0, v3
	s_and_b64 s[58:59], s[46:47], s[0:1]
	v_cmp_gt_f32_e64 s[0:1], v34, v2
	s_and_b64 s[0:1], s[58:59], s[0:1]
	v_and_b32_e32 v3, 16, v0
	v_cndmask_b32_e64 v1, v1, 3, s[0:1]
	v_cndmask_b32_e64 v2, v2, v34, s[0:1]
	v_cmp_eq_u32_e64 s[0:1], 0, v3
	s_and_b64 s[58:59], s[48:49], s[0:1]
	v_cmp_gt_f32_e64 s[0:1], v37, v2
	s_and_b64 s[0:1], s[58:59], s[0:1]
	v_and_b32_e32 v3, 32, v0
	v_cndmask_b32_e64 v1, v1, 4, s[0:1]
	v_cndmask_b32_e64 v2, v2, v37, s[0:1]
	v_cmp_eq_u32_e64 s[0:1], 0, v3
	s_and_b64 s[58:59], s[50:51], s[0:1]
	v_cmp_gt_f32_e64 s[0:1], v36, v2
	s_and_b64 s[0:1], s[58:59], s[0:1]
	v_and_b32_e32 v3, 64, v0
	v_cndmask_b32_e64 v1, v1, 5, s[0:1]
	v_cndmask_b32_e64 v2, v2, v36, s[0:1]
	v_cmp_eq_u32_e64 s[0:1], 0, v3
	s_and_b64 s[58:59], s[52:53], s[0:1]
	v_cmp_gt_f32_e64 s[0:1], v38, v2
	s_and_b64 s[0:1], s[58:59], s[0:1]
	v_mov_b32_e32 v9, v117
	v_cndmask_b32_e64 v1, v1, 6, s[0:1]
	v_lshlrev_b32_e64 v2, v1, 1
	v_cmp_lt_i32_e64 s[0:1], -1, v1
	v_mov_b32_e32 v10, v117
	v_mov_b32_e32 v11, v117
	v_cndmask_b32_e64 v1, 0, v2, s[0:1]
	v_or_b32_e32 v2, v1, v0
	v_and_b32_e32 v3, 1, v2
	v_cmp_eq_u32_e64 s[0:1], 1, v3
	s_or_b64 vcc, vcc, s[0:1]
	v_bitop3_b32 v5, v1, 2, v0 bitop3:0xc8
	v_cndmask_b32_e64 v3, 0, -1, vcc
	v_cndmask_b32_e32 v4, v17, v192, vcc
	v_cmp_eq_u32_e32 vcc, 0, v5
	s_and_b64 s[0:1], s[6:7], vcc
	v_cmp_gt_f32_e32 vcc, v16, v4
	s_and_b64 vcc, s[0:1], vcc
	v_bitop3_b32 v5, v1, 4, v0 bitop3:0xc8
	v_cndmask_b32_e64 v3, v3, 1, vcc
	v_cndmask_b32_e32 v4, v4, v16, vcc
	v_cmp_eq_u32_e32 vcc, 0, v5
	s_and_b64 s[0:1], s[44:45], vcc
	v_cmp_gt_f32_e32 vcc, v35, v4
	s_and_b64 vcc, s[0:1], vcc
	v_bitop3_b32 v5, v1, 8, v0 bitop3:0xc8
	v_cndmask_b32_e64 v3, v3, 2, vcc
	v_cndmask_b32_e32 v4, v4, v35, vcc
	v_cmp_eq_u32_e32 vcc, 0, v5
	s_and_b64 s[0:1], s[46:47], vcc
	v_cmp_gt_f32_e32 vcc, v34, v4
	s_and_b64 vcc, s[0:1], vcc
	v_bitop3_b32 v5, v1, 16, v0 bitop3:0xc8
	v_cndmask_b32_e64 v3, v3, 3, vcc
	v_cndmask_b32_e32 v4, v4, v34, vcc
	v_cmp_eq_u32_e32 vcc, 0, v5
	s_and_b64 s[0:1], s[48:49], vcc
	v_cmp_gt_f32_e32 vcc, v37, v4
	s_and_b64 vcc, s[0:1], vcc
	v_bitop3_b32 v5, v1, 32, v0 bitop3:0xc8
	v_cndmask_b32_e64 v3, v3, 4, vcc
	v_cndmask_b32_e32 v4, v4, v37, vcc
	v_cmp_eq_u32_e32 vcc, 0, v5
	s_and_b64 s[0:1], s[50:51], vcc
	v_cmp_gt_f32_e32 vcc, v36, v4
	s_and_b64 vcc, s[0:1], vcc
	v_bitop3_b32 v0, v1, 64, v0 bitop3:0xc8
	v_cndmask_b32_e64 v3, v3, 5, vcc
	v_cndmask_b32_e32 v4, v4, v36, vcc
	v_cmp_eq_u32_e32 vcc, 0, v0
	s_and_b64 s[0:1], s[52:53], vcc
	v_cmp_gt_f32_e32 vcc, v38, v4
	s_and_b64 s[0:1], s[0:1], vcc
	v_cndmask_b32_e64 v0, v3, 6, s[0:1]
	v_lshlrev_b32_e64 v1, v0, 1
	v_cmp_lt_i32_e32 vcc, -1, v0
	s_lshl_b32 s0, s33, 2
	s_or_b32 s48, s8, 31
	v_cndmask_b32_e32 v0, 0, v1, vcc
	s_sub_i32 s49, 31, s0
	s_lshl_b32 s0, s33, 8
	v_or_b32_e32 v198, v0, v2
	v_mov_b32_e32 v0, v137
	v_subrev_u32_e32 v200, s0, v171
	s_add_u32 s0, s54, s55
	v_mul_f32_e32 v142, s14, v0
	v_mul_f32_e32 v143, s15, v0
	v_mul_f32_e32 v144, s24, v0
	v_mul_f32_e32 v145, s25, v0
	v_mul_f32_e32 v146, s26, v0
	v_mul_f32_e32 v147, s27, v0
	v_mul_f32_e32 v148, s34, v0
	v_mul_f32_e32 v149, s35, v0
	v_mul_f32_e32 v150, s36, v0
	v_mul_f32_e32 v151, s37, v0
	v_mul_f32_e32 v152, s38, v0
	v_mul_f32_e32 v153, s39, v0
	v_mul_f32_e32 v154, s40, v0
	v_mul_f32_e32 v155, s41, v0
	s_addc_u32 s1, 0, 0
	v_mov_b32_e32 v0, v117
	v_mov_b32_e32 v1, v117
	v_mov_b32_e32 v2, v117
	v_mov_b32_e32 v3, v117
	v_mov_b32_e32 v4, v117
	v_mov_b32_e32 v5, v117
	v_mov_b32_e32 v12, v117
	v_mov_b32_e32 v13, v117
	v_mov_b64_e32 v[30:31], v[14:15]
	s_mov_b32 s56, 0
	v_mul_f32_e32 v136, 0, v137
	v_sub_u32_e32 v199, v164, v195
	v_mov_b32_e32 v140, v138
	v_mov_b32_e32 v141, v138
	v_lshl_add_u64 v[156:157], v[132:133], 0, s[0:1]
	v_lshl_add_u64 v[158:159], v[134:135], 0, s[0:1]
	s_movk_i32 s50, 0x4000
	s_mov_b64 s[44:45], 0
	v_mov_b64_e32 v[28:29], v[12:13]
	v_mov_b64_e32 v[26:27], v[10:11]
	v_mov_b64_e32 v[24:25], v[8:9]
	v_mov_b64_e32 v[22:23], v[6:7]
	v_mov_b64_e32 v[20:21], v[4:5]
	v_mov_b64_e32 v[18:19], v[2:3]
	v_mov_b64_e32 v[16:17], v[0:1]
	v_mov_b32_e32 v196, 0
	s_mov_b32 s33, 0
	s_mov_b32 s51, 0
	s_branch .LBB0_487

.Lmoba0_a:
	v_and_b32_e32 v33, s6, v198
	v_cmp_ne_u32_e32 vcc, 0, v33
	v_fma_f32 v32, v137, v32, -v197
	s_or_b64 vcc, s[0:1], vcc
	v_cndmask_b32_e32 v32, v192, v32, vcc
	v_add_f32_e32 v48, v136, v32
	v_add_f32_e32 v49, v137, v32
	v_add_f32_e32 v50, v142, v32
	v_add_f32_e32 v51, v143, v32
	v_add_f32_e32 v52, v144, v32
	v_add_f32_e32 v53, v145, v32
	v_add_f32_e32 v54, v146, v32
	v_add_f32_e32 v55, v147, v32
	v_add_f32_e32 v56, v148, v32
	v_add_f32_e32 v57, v149, v32
	v_add_f32_e32 v58, v150, v32
	v_add_f32_e32 v59, v151, v32
	v_add_f32_e32 v60, v152, v32
	v_add_f32_e32 v61, v153, v32
	v_add_f32_e32 v62, v154, v32
	v_add_f32_e32 v63, v155, v32
	v_mov_b32_e32 v139, v138
	v_add_f32_e32 v46, v138, v62
	v_add_f32_e32 v47, v139, v63
	v_add_f32_e32 v44, v138, v60
	v_add_f32_e32 v45, v139, v61
	v_add_f32_e32 v42, v138, v58
	v_add_f32_e32 v43, v139, v59
	v_add_f32_e32 v40, v138, v56
	v_add_f32_e32 v41, v139, v57
	v_add_f32_e32 v38, v138, v54
	v_add_f32_e32 v39, v139, v55
	v_add_f32_e32 v36, v138, v52
	v_add_f32_e32 v37, v139, v53
	v_add_f32_e32 v34, v138, v50
	v_add_f32_e32 v35, v139, v51
	v_add_f32_e32 v32, v140, v48
	v_add_f32_e32 v33, v141, v49
	v_add_u32_e32 v139, s33, v166
	ds_read_b64_tr_b16 v[100:101], v139 offset:24576
	ds_read_b64_tr_b16 v[102:103], v139 offset:25088
	ds_read_b64_tr_b16 v[92:93], v139 offset:25600
	ds_read_b64_tr_b16 v[94:95], v139 offset:26112
	ds_read_b128 v[104:107], v160 offset:4096
	ds_read_b128 v[108:111], v160 offset:4608
	s_waitcnt lgkmcnt(0)
	v_mfma_f32_32x32x16_bf16 v[48:63], v[80:83], v[76:79], v[48:63]
	v_mfma_f32_32x32x16_bf16 v[32:47], v[84:87], v[76:79], v[32:47]
	ds_read_b64_tr_b16 v[84:85], v139 offset:26624
	ds_read_b64_tr_b16 v[86:87], v139 offset:27136
	ds_read_b64_tr_b16 v[80:81], v139 offset:27648
	ds_read_b64_tr_b16 v[82:83], v139 offset:28160
	ds_read_b128 v[202:205], v160 offset:6144
	ds_read_b128 v[206:209], v160 offset:6656
	v_mfma_f32_32x32x16_bf16 v[48:63], v[88:91], v[72:75], v[48:63]
	v_mfma_f32_32x32x16_bf16 v[32:47], v[96:99], v[72:75], v[32:47]
	v_mfma_f32_32x32x16_bf16 v[48:63], v[104:107], v[68:71], v[48:63]
	v_mfma_f32_32x32x16_bf16 v[32:47], v[108:111], v[68:71], v[32:47]
	s_waitcnt lgkmcnt(0)
	v_mfma_f32_32x32x16_bf16 v[48:63], v[202:205], v[64:67], v[48:63]
	ds_read_b64_tr_b16 v[108:109], v139 offset:28672
	ds_read_b64_tr_b16 v[110:111], v139 offset:29184
	ds_read_b64_tr_b16 v[104:105], v139 offset:29696
	ds_read_b64_tr_b16 v[106:107], v139 offset:30208
	v_mfma_f32_32x32x16_bf16 v[32:47], v[206:209], v[64:67], v[32:47]
	ds_read_b64_tr_b16 v[96:97], v139 offset:30720
	ds_read_b64_tr_b16 v[98:99], v139 offset:31232
	ds_read_b64_tr_b16 v[88:89], v139 offset:31744
	ds_read_b64_tr_b16 v[90:91], v139 offset:32256
	s_add_i32 s6, s56, 63
	s_cmp_gt_u32 s6, s8
	s_cselect_b64 s[6:7], -1, 0
	s_and_b64 s[0:1], s[0:1], s[6:7]
	s_andn2_b64 vcc, exec, s[0:1]
	s_cbranch_vccnz .LBB0_496
	v_add_u32_e32 v139, 27, v200
	v_cmp_lt_i32_e32 vcc, -1, v139
	s_nop 1
	v_cndmask_b32_e32 v48, v192, v48, vcc
	v_cmp_lt_i32_e32 vcc, 31, v139
	v_add_u32_e32 v139, 26, v200
	s_nop 0
	v_cndmask_b32_e32 v32, v192, v32, vcc
	v_cmp_lt_i32_e32 vcc, -1, v139
	s_nop 1
	v_cndmask_b32_e32 v49, v192, v49, vcc
	v_cmp_lt_i32_e32 vcc, 31, v139
	v_add_u32_e32 v139, 25, v200
	s_nop 0
	v_cndmask_b32_e32 v33, v192, v33, vcc
	v_cmp_lt_i32_e32 vcc, -1, v139
	s_nop 1
	v_cndmask_b32_e32 v50, v192, v50, vcc
	v_cmp_lt_i32_e32 vcc, 31, v139
	v_add_u32_e32 v139, 24, v200
	s_nop 0
	v_cndmask_b32_e32 v34, v192, v34, vcc
	v_cmp_lt_i32_e32 vcc, -1, v139
	s_nop 1
	v_cndmask_b32_e32 v51, v192, v51, vcc
	v_cmp_lt_i32_e32 vcc, 31, v139
	v_add_u32_e32 v139, 19, v200
	s_nop 0
	v_cndmask_b32_e32 v35, v192, v35, vcc
	v_cmp_lt_i32_e32 vcc, -1, v139
	s_nop 1
	v_cndmask_b32_e32 v52, v192, v52, vcc
	v_cmp_lt_i32_e32 vcc, 31, v139
	v_add_u32_e32 v139, 18, v200
	s_nop 0
	v_cndmask_b32_e32 v36, v192, v36, vcc
	v_cmp_lt_i32_e32 vcc, -1, v139
	s_nop 1
	v_cndmask_b32_e32 v53, v192, v53, vcc
	v_cmp_lt_i32_e32 vcc, 31, v139
	v_add_u32_e32 v139, 17, v200
	s_nop 0
	v_cndmask_b32_e32 v37, v192, v37, vcc
	v_cmp_lt_i32_e32 vcc, -1, v139
	s_nop 1
	v_cndmask_b32_e32 v54, v192, v54, vcc
	v_cmp_lt_i32_e32 vcc, 31, v139
	v_add_u32_e32 v139, 16, v200
	s_nop 0
	v_cndmask_b32_e32 v38, v192, v38, vcc
	v_cmp_lt_i32_e32 vcc, -1, v139
	s_nop 1
	v_cndmask_b32_e32 v55, v192, v55, vcc
	v_cmp_lt_i32_e32 vcc, 31, v139
	v_add_u32_e32 v139, 11, v200
	s_nop 0
	v_cndmask_b32_e32 v39, v192, v39, vcc
	v_cmp_lt_i32_e32 vcc, -1, v139
	s_nop 1
	v_cndmask_b32_e32 v56, v192, v56, vcc
	v_cmp_lt_i32_e32 vcc, 31, v139
	v_add_u32_e32 v139, 10, v200
	s_nop 0
	v_cndmask_b32_e32 v40, v192, v40, vcc
	v_cmp_lt_i32_e32 vcc, -1, v139
	s_nop 1
	v_cndmask_b32_e32 v57, v192, v57, vcc
	v_cmp_lt_i32_e32 vcc, 31, v139
	v_add_u32_e32 v139, 9, v200
	s_nop 0
	v_cndmask_b32_e32 v41, v192, v41, vcc
	v_cmp_lt_i32_e32 vcc, -1, v139
	s_nop 1
	v_cndmask_b32_e32 v58, v192, v58, vcc
	v_cmp_lt_i32_e32 vcc, 31, v139
	v_add_u32_e32 v139, 8, v200
	s_nop 0
	v_cndmask_b32_e32 v42, v192, v42, vcc
	v_cmp_lt_i32_e32 vcc, -1, v139
	s_nop 1
	v_cndmask_b32_e32 v59, v192, v59, vcc
	v_cmp_lt_i32_e32 vcc, 31, v139
	v_add_u32_e32 v139, 3, v200
	s_nop 0
	v_cndmask_b32_e32 v43, v192, v43, vcc
	v_cmp_lt_i32_e32 vcc, -1, v139
	s_nop 1
	v_cndmask_b32_e32 v60, v192, v60, vcc
	v_cmp_lt_i32_e32 vcc, 31, v139
	v_add_u32_e32 v139, 2, v200
	s_nop 0
	v_cndmask_b32_e32 v44, v192, v44, vcc
	v_cmp_lt_i32_e32 vcc, -1, v139
	s_nop 1
	v_cndmask_b32_e32 v61, v192, v61, vcc
	v_cmp_lt_i32_e32 vcc, 31, v139
	v_add_u32_e32 v139, 1, v200
	s_nop 0
	v_cndmask_b32_e32 v45, v192, v45, vcc
	v_cmp_lt_i32_e32 vcc, -1, v139
	s_nop 1
	v_cndmask_b32_e32 v62, v192, v62, vcc
	v_cmp_lt_i32_e32 vcc, 31, v139
	s_nop 1
	v_cndmask_b32_e32 v46, v192, v46, vcc
	v_cmp_lt_i32_e32 vcc, -1, v200
	s_nop 1
	v_cndmask_b32_e32 v63, v192, v63, vcc
	v_cmp_lt_i32_e32 vcc, 31, v200
	s_nop 1
	v_cndmask_b32_e32 v47, v192, v47, vcc
.LBB0_496:
	v_max_f32_e32 v139, v49, v49
	v_max_f32_e32 v160, v48, v48
	v_max_f32_e32 v139, v160, v139
	v_max3_f32 v160, v50, v51, v33
	v_max3_f32 v139, v139, v32, v34
	v_max3_f32 v139, v139, v35, v52
	v_max3_f32 v160, v160, v54, v55
	v_max3_f32 v139, v139, v53, v36
	v_max3_f32 v160, v160, v38, v39
	v_max3_f32 v139, v139, v37, v56
	v_max3_f32 v160, v160, v58, v59
	v_max3_f32 v139, v139, v57, v40
	v_max3_f32 v160, v160, v42, v43
	v_max3_f32 v139, v139, v41, v60
	v_max3_f32 v160, v160, v62, v63
	v_max3_f32 v139, v139, v61, v44
	v_max3_f32 v160, v160, v46, v47
	v_max3_f32 v139, v139, v45, v160
	v_mov_b32_e32 v160, v139
	s_nop 1
	v_permlane32_swap_b32_e32 v139, v160
	v_max_f32_e32 v160, v160, v160
	v_max_f32_e32 v139, v139, v139
	v_max_f32_e32 v139, v139, v160
	v_cmp_lg_f32_e64 s[0:1], s23, v139
	s_xor_b64 s[6:7], s[44:45], -1
	s_and_b64 s[6:7], s[0:1], s[6:7]
	v_cmp_lt_f32_e32 vcc, s24, v139
	s_or_b64 s[52:53], vcc, s[6:7]
	v_cndmask_b32_e64 v160, 0, 1, s[52:53]
	v_cmp_ne_u32_e32 vcc, 0, v160
	s_cbranch_vccz .LBB0_500
	v_cndmask_b32_e64 v160, 0, v139, s[6:7]
	v_max_f32_e32 v139, v139, v139
	v_max_f32_e32 v139, 0, v139
	v_cndmask_b32_e64 v160, v160, v139, s[44:45]
	v_exp_f32_e64 v139, -v160
	s_nop 0
	v_cndmask_b32_e64 v139, v139, 1.0, s[6:7]
	s_and_saveexec_b64 s[6:7], s[4:5]
	ds_write_b32 v167, v139 offset:49152
	s_or_b64 exec, exec, s[6:7]
	s_waitcnt lgkmcnt(0)
	ds_read_b128 v[202:205], v168 offset:49152
	ds_read_b128 v[206:209], v168 offset:49184
	ds_read_b128 v[210:213], v168 offset:49216
	ds_read_b128 v[214:217], v168 offset:49248
	v_mul_f32_e32 v196, v196, v139
	v_add_f32_e64 v48, v48, -v160
	v_add_f32_e64 v49, v49, -v160
	v_add_f32_e64 v32, v32, -v160
	v_add_f32_e64 v33, v33, -v160
	v_add_f32_e64 v50, v50, -v160
	v_add_f32_e64 v51, v51, -v160
	v_add_f32_e64 v34, v34, -v160
	v_add_f32_e64 v35, v35, -v160
	v_add_f32_e64 v52, v52, -v160
	v_add_f32_e64 v53, v53, -v160
	v_add_f32_e64 v36, v36, -v160
	v_add_f32_e64 v37, v37, -v160
	v_add_f32_e64 v54, v54, -v160
	v_add_f32_e64 v55, v55, -v160
	v_add_f32_e64 v38, v38, -v160
	v_add_f32_e64 v39, v39, -v160
	v_add_f32_e64 v56, v56, -v160
	v_add_f32_e64 v57, v57, -v160
	v_add_f32_e64 v40, v40, -v160
	v_add_f32_e64 v41, v41, -v160
	v_add_f32_e64 v58, v58, -v160
	v_add_f32_e64 v59, v59, -v160
	v_add_f32_e64 v42, v42, -v160
	v_add_f32_e64 v43, v43, -v160
	v_add_f32_e64 v60, v60, -v160
	v_add_f32_e64 v61, v61, -v160
	v_add_f32_e64 v44, v44, -v160
	v_add_f32_e64 v45, v45, -v160
	v_add_f32_e64 v62, v62, -v160
	v_add_f32_e64 v63, v63, -v160
	v_add_f32_e64 v46, v46, -v160
	v_add_f32_e64 v47, v47, -v160
	v_add_f32_e32 v197, v197, v160
	s_or_b64 s[44:45], s[44:45], s[0:1]
	s_waitcnt lgkmcnt(0)
	v_mul_f32_e32 v14, v14, v216
	v_mul_f32_e32 v15, v15, v217
	v_mul_f32_e32 v10, v10, v212
	v_mul_f32_e32 v11, v11, v213
	v_mul_f32_e32 v6, v6, v208
	v_mul_f32_e32 v7, v7, v209
	v_mul_f32_e32 v2, v2, v204
	v_mul_f32_e32 v3, v3, v205
	v_mul_f32_e32 v12, v12, v214
	v_mul_f32_e32 v13, v13, v215
	v_mul_f32_e32 v8, v8, v210
	v_mul_f32_e32 v9, v9, v211
	v_mul_f32_e32 v4, v4, v206
	v_mul_f32_e32 v5, v5, v207
	v_mul_f32_e32 v0, v0, v202
	v_mul_f32_e32 v1, v1, v203
	v_mul_f32_e32 v30, v30, v216
	v_mul_f32_e32 v31, v31, v217
	v_mul_f32_e32 v26, v26, v212
	v_mul_f32_e32 v27, v27, v213
	v_mul_f32_e32 v22, v22, v208
	v_mul_f32_e32 v23, v23, v209
	v_mul_f32_e32 v18, v18, v204
	v_mul_f32_e32 v19, v19, v205
	v_mul_f32_e32 v28, v28, v214
	v_mul_f32_e32 v29, v29, v215
	v_mul_f32_e32 v24, v24, v210
	v_mul_f32_e32 v25, v25, v211
	v_mul_f32_e32 v20, v20, v206
	v_mul_f32_e32 v21, v21, v207
	v_mul_f32_e32 v16, v16, v202
	v_mul_f32_e32 v17, v17, v203
.LBB0_500:
	v_exp_f32_e32 v203, v48
	v_exp_f32_e32 v202, v32
	v_exp_f32_e32 v49, v49
	v_exp_f32_e32 v48, v33
	v_exp_f32_e32 v205, v50
	v_exp_f32_e32 v204, v34
	v_exp_f32_e32 v51, v51
	v_exp_f32_e32 v50, v35
	v_exp_f32_e32 v209, v52
	v_exp_f32_e32 v53, v53
	v_exp_f32_e32 v211, v54
	v_exp_f32_e32 v55, v55
	v_cvt_pk_bf16_f32 v32, v203, v49
	v_cvt_pk_bf16_f32 v33, v205, v51
	v_cvt_pk_bf16_f32 v34, v209, v53
	v_cvt_pk_bf16_f32 v35, v211, v55
	v_add_f32_e32 v206, 0, v202
	v_add_f32_e32 v207, 0, v203
	v_mfma_f32_32x32x16_bf16 v[0:15], v[32:35], v[100:103], v[0:15]
	v_add_f32_e64 v100, v48, v206
	v_add_f32_e64 v101, v49, v207
	v_exp_f32_e32 v103, v56
	v_exp_f32_e32 v57, v57
	v_exp_f32_e32 v207, v58
	v_exp_f32_e32 v59, v59
	v_exp_f32_e32 v213, v60
	v_exp_f32_e32 v49, v61
	s_waitcnt lgkmcnt(0)
	v_mfma_f32_32x32x16_bf16 v[16:31], v[32:35], v[108:111], v[16:31]
	v_exp_f32_e32 v61, v62
	v_exp_f32_e32 v63, v63
	v_cvt_pk_bf16_f32 v32, v103, v57
	v_cvt_pk_bf16_f32 v33, v207, v59
	v_cvt_pk_bf16_f32 v34, v213, v49
	v_cvt_pk_bf16_f32 v35, v61, v63
	v_exp_f32_e32 v208, v36
	v_mfma_f32_32x32x16_bf16 v[0:15], v[32:35], v[92:95], v[0:15]
	v_exp_f32_e32 v52, v37
	v_add_f32_e32 v100, v204, v100
	v_add_f32_e32 v101, v205, v101
	v_exp_f32_e32 v210, v38
	v_exp_f32_e32 v54, v39
	v_add_f32_e32 v92, v50, v100
	v_add_f32_e32 v93, v51, v101
	v_exp_f32_e32 v102, v40
	v_add_f32_e32 v36, v208, v92
	v_add_f32_e32 v37, v209, v93
	v_mfma_f32_32x32x16_bf16 v[16:31], v[32:35], v[104:107], v[16:31]
	v_cvt_pk_bf16_f32 v32, v202, v48
	v_cvt_pk_bf16_f32 v33, v204, v50
	v_cvt_pk_bf16_f32 v34, v208, v52
	v_cvt_pk_bf16_f32 v35, v210, v54
	v_exp_f32_e32 v56, v41
	v_add_f32_e32 v36, v52, v36
	v_add_f32_e32 v37, v53, v37
	v_exp_f32_e32 v206, v42
	v_mfma_f32_32x32x16_bf16 v[0:15], v[32:35], v[84:87], v[0:15]
	v_add_f32_e64 v36, v210, v36
	v_add_f32_e64 v37, v211, v37
	v_exp_f32_e32 v58, v43
	v_add_f32_e32 v36, v54, v36
	v_add_f32_e32 v37, v55, v37
	v_exp_f32_e32 v212, v44
	v_exp_f32_e32 v48, v45
	v_exp_f32_e32 v60, v46
	v_exp_f32_e32 v62, v47
	v_mfma_f32_32x32x16_bf16 v[16:31], v[32:35], v[96:99], v[16:31]
	v_add_f32_e64 v32, v102, v36
	v_add_f32_e64 v33, v103, v37
	s_andn2_b64 s[0:1], s[46:47], exec
	v_add_f32_e64 v32, v56, v32
	v_add_f32_e64 v33, v57, v33
	s_and_b64 s[6:7], s[44:45], exec
	v_add_f32_e32 v36, v206, v32
	v_add_f32_e32 v37, v207, v33
	v_cvt_pk_bf16_f32 v32, v102, v56
	v_cvt_pk_bf16_f32 v33, v206, v58
	v_cvt_pk_bf16_f32 v34, v212, v48
	v_cvt_pk_bf16_f32 v35, v60, v62
	s_or_b64 s[44:45], s[0:1], s[6:7]
	v_mfma_f32_32x32x16_bf16 v[0:15], v[32:35], v[80:83], v[0:15]
	v_add_f32_e64 v36, v58, v36
	v_add_f32_e64 v37, v59, v37
	v_add_f32_e64 v36, v212, v36
	v_add_f32_e64 v37, v213, v37
	v_add_f32_e64 v36, v48, v36
	v_add_f32_e64 v37, v49, v37
	v_add_f32_e32 v36, v60, v36
	v_add_f32_e32 v37, v61, v37
	v_mfma_f32_32x32x16_bf16 v[16:31], v[32:35], v[88:91], v[16:31]
	v_add_f32_e64 v36, v62, v36
	v_add_f32_e64 v37, v63, v37
	v_add_f32_e32 v36, v36, v37
	v_add_f32_e32 v196, v196, v36
	s_branch .LBB0_486

.LBB0_506:
	v_add_u32_e32 v32, s30, v199
	v_cvt_f32_i32_e32 v32, v32
	s_lshl_b32 s6, 1, s50
	v_and_b32_e32 v33, s6, v198
	v_cmp_ne_u32_e32 vcc, 0, v33
	v_fma_f32 v32, v137, v32, -v197
	s_or_b64 vcc, s[0:1], vcc
	v_cndmask_b32_e32 v32, v192, v32, vcc
	v_add_f32_e32 v48, v136, v32
	v_add_f32_e32 v49, v137, v32
	v_add_u32_e32 v136, s33, v165
	ds_read_b128 v[80:83], v136
	ds_read_b128 v[92:95], v136 offset:512
	ds_read_b128 v[96:99], v136 offset:2048
	ds_read_b128 v[100:103], v136 offset:2560
	v_add_f32_e32 v50, v142, v32
	v_add_f32_e32 v51, v143, v32
	v_add_f32_e32 v52, v144, v32
	v_add_f32_e32 v53, v145, v32
	v_add_f32_e32 v54, v146, v32
	v_add_f32_e32 v55, v147, v32
	v_add_f32_e32 v56, v148, v32
	v_add_f32_e32 v57, v149, v32
	v_add_f32_e32 v58, v150, v32
	v_add_f32_e32 v59, v151, v32
	v_add_f32_e32 v60, v152, v32
	v_add_f32_e32 v61, v153, v32
	v_add_f32_e32 v62, v154, v32
	v_add_f32_e32 v63, v155, v32
	v_mov_b32_e32 v139, v138
	v_add_f32_e32 v46, v138, v62
	v_add_f32_e32 v47, v139, v63
	v_add_f32_e32 v44, v138, v60
	v_add_f32_e32 v45, v139, v61
	v_add_f32_e32 v42, v138, v58
	v_add_f32_e32 v43, v139, v59
	v_add_f32_e32 v40, v138, v56
	v_add_f32_e32 v41, v139, v57
	v_add_f32_e32 v38, v138, v54
	v_add_f32_e32 v39, v139, v55
	v_add_f32_e32 v36, v138, v52
	v_add_f32_e32 v37, v139, v53
	v_add_f32_e32 v34, v138, v50
	v_add_f32_e32 v35, v139, v51
	v_add_f32_e32 v32, v140, v48
	v_add_f32_e32 v33, v141, v49
	v_add_u32_e32 v140, s33, v166
	ds_read_b64_tr_b16 v[88:89], v140 offset:24576
	ds_read_b64_tr_b16 v[90:91], v140 offset:25088
	ds_read_b64_tr_b16 v[84:85], v140 offset:25600
	ds_read_b64_tr_b16 v[86:87], v140 offset:26112
	ds_read_b128 v[104:107], v136 offset:4096
	ds_read_b128 v[108:111], v136 offset:4608
	s_waitcnt lgkmcnt(0)
	v_mfma_f32_32x32x16_bf16 v[48:63], v[80:83], v[76:79], v[48:63]
	v_mfma_f32_32x32x16_bf16 v[32:47], v[92:95], v[76:79], v[32:47]
	ds_read_b64_tr_b16 v[80:81], v140 offset:26624
	ds_read_b64_tr_b16 v[82:83], v140 offset:27136
	ds_read_b64_tr_b16 v[76:77], v140 offset:27648
	ds_read_b64_tr_b16 v[78:79], v140 offset:28160
	ds_read_b128 v[92:95], v136 offset:6144
	ds_read_b128 v[136:139], v136 offset:6656
	v_mfma_f32_32x32x16_bf16 v[48:63], v[96:99], v[72:75], v[48:63]
	v_mfma_f32_32x32x16_bf16 v[32:47], v[100:103], v[72:75], v[32:47]
	v_mfma_f32_32x32x16_bf16 v[48:63], v[104:107], v[68:71], v[48:63]
	v_mfma_f32_32x32x16_bf16 v[32:47], v[108:111], v[68:71], v[32:47]
	s_waitcnt lgkmcnt(0)
	v_mfma_f32_32x32x16_bf16 v[48:63], v[92:95], v[64:67], v[48:63]
	ds_read_b64_tr_b16 v[92:93], v140 offset:28672
	ds_read_b64_tr_b16 v[94:95], v140 offset:29184
	ds_read_b64_tr_b16 v[72:73], v140 offset:29696
	ds_read_b64_tr_b16 v[74:75], v140 offset:30208
	v_mfma_f32_32x32x16_bf16 v[32:47], v[136:139], v[64:67], v[32:47]
	ds_read_b64_tr_b16 v[68:69], v140 offset:30720
	ds_read_b64_tr_b16 v[70:71], v140 offset:31232
	ds_read_b64_tr_b16 v[64:65], v140 offset:31744
	ds_read_b64_tr_b16 v[66:67], v140 offset:32256
	s_or_b32 s6, s30, 63
	s_cmp_gt_u32 s6, s8
	s_cselect_b64 s[6:7], -1, 0
	s_and_b64 s[0:1], s[0:1], s[6:7]
	s_andn2_b64 vcc, exec, s[0:1]
	s_cbranch_vccnz .LBB0_508
	v_add_u32_e32 v96, s30, v164
	v_sub_u32_e32 v97, v195, v96
	v_cmp_lt_i32_e32 vcc, -1, v97
	v_xad_u32 v98, v96, -1, v195
	s_nop 0
	v_cndmask_b32_e32 v48, v192, v48, vcc
	v_cmp_lt_i32_e32 vcc, 31, v97
	s_nop 1
	v_cndmask_b32_e32 v32, v192, v32, vcc
	v_cmp_lt_i32_e32 vcc, -1, v98
	s_nop 1
	v_cndmask_b32_e32 v49, v192, v49, vcc
	v_cmp_lt_i32_e32 vcc, 31, v98
	v_or_b32_e32 v98, 2, v96
	v_sub_u32_e32 v98, v195, v98
	v_cndmask_b32_e32 v33, v192, v33, vcc
	v_cmp_lt_i32_e32 vcc, -1, v98
	v_or_b32_e32 v96, 3, v96
	v_sub_u32_e32 v96, v195, v96
	v_cndmask_b32_e32 v50, v192, v50, vcc
	v_cmp_lt_i32_e32 vcc, 31, v98
	s_nop 1
	v_cndmask_b32_e32 v34, v192, v34, vcc
	v_cmp_lt_i32_e32 vcc, -1, v96
	s_nop 1
	v_cndmask_b32_e32 v51, v192, v51, vcc
	v_cmp_lt_i32_e32 vcc, 31, v96
	v_add_u32_e32 v96, -8, v97
	s_nop 0
	v_cndmask_b32_e32 v35, v192, v35, vcc
	v_cmp_lt_i32_e32 vcc, -1, v96
	s_nop 1
	v_cndmask_b32_e32 v52, v192, v52, vcc
	v_cmp_lt_i32_e32 vcc, 31, v96
	v_add_u32_e32 v96, -9, v97
	s_nop 0
	v_cndmask_b32_e32 v36, v192, v36, vcc
	v_cmp_lt_i32_e32 vcc, -1, v96
	s_nop 1
	v_cndmask_b32_e32 v53, v192, v53, vcc
	v_cmp_lt_i32_e32 vcc, 31, v96
	v_add_u32_e32 v96, -10, v97
	s_nop 0
	v_cndmask_b32_e32 v37, v192, v37, vcc
	v_cmp_lt_i32_e32 vcc, -1, v96
	s_nop 1
	v_cndmask_b32_e32 v54, v192, v54, vcc
	v_cmp_lt_i32_e32 vcc, 31, v96
	v_add_u32_e32 v96, -11, v97
	s_nop 0
	v_cndmask_b32_e32 v38, v192, v38, vcc
	v_cmp_lt_i32_e32 vcc, -1, v96
	s_nop 1
	v_cndmask_b32_e32 v55, v192, v55, vcc
	v_cmp_lt_i32_e32 vcc, 31, v96
	v_add_u32_e32 v96, -16, v97
	s_nop 0
	v_cndmask_b32_e32 v39, v192, v39, vcc
	v_cmp_lt_i32_e32 vcc, -1, v96
	s_nop 1
	v_cndmask_b32_e32 v56, v192, v56, vcc
	v_cmp_lt_i32_e32 vcc, 31, v96
	v_subrev_u32_e32 v96, 17, v97
	s_nop 0
	v_cndmask_b32_e32 v40, v192, v40, vcc
	v_cmp_lt_i32_e32 vcc, -1, v96
	s_nop 1
	v_cndmask_b32_e32 v57, v192, v57, vcc
	v_cmp_lt_i32_e32 vcc, 31, v96
	v_subrev_u32_e32 v96, 18, v97
	s_nop 0
	v_cndmask_b32_e32 v41, v192, v41, vcc
	v_cmp_lt_i32_e32 vcc, -1, v96
	s_nop 1
	v_cndmask_b32_e32 v58, v192, v58, vcc
	v_cmp_lt_i32_e32 vcc, 31, v96
	v_subrev_u32_e32 v96, 19, v97
	s_nop 0
	v_cndmask_b32_e32 v42, v192, v42, vcc
	v_cmp_lt_i32_e32 vcc, -1, v96
	s_nop 1
	v_cndmask_b32_e32 v59, v192, v59, vcc
	v_cmp_lt_i32_e32 vcc, 31, v96
	v_subrev_u32_e32 v96, 24, v97
	s_nop 0
	v_cndmask_b32_e32 v43, v192, v43, vcc
	v_cmp_lt_i32_e32 vcc, -1, v96
	s_nop 1
	v_cndmask_b32_e32 v60, v192, v60, vcc
	v_cmp_lt_i32_e32 vcc, 31, v96
	v_subrev_u32_e32 v96, 25, v97
	s_nop 0
	v_cndmask_b32_e32 v44, v192, v44, vcc
	v_cmp_lt_i32_e32 vcc, -1, v96
	s_nop 1
	v_cndmask_b32_e32 v61, v192, v61, vcc
	v_cmp_lt_i32_e32 vcc, 31, v96
	v_subrev_u32_e32 v96, 26, v97
	s_nop 0
	v_cndmask_b32_e32 v45, v192, v45, vcc
	v_cmp_lt_i32_e32 vcc, -1, v96
	s_nop 1
	v_cndmask_b32_e32 v62, v192, v62, vcc
	v_cmp_lt_i32_e32 vcc, 31, v96
	v_subrev_u32_e32 v96, 27, v97
	s_nop 0
	v_cndmask_b32_e32 v46, v192, v46, vcc
	v_cmp_lt_i32_e32 vcc, -1, v96
	s_nop 1
	v_cndmask_b32_e32 v63, v192, v63, vcc
	v_cmp_lt_i32_e32 vcc, 31, v96
	s_nop 1
	v_cndmask_b32_e32 v47, v192, v47, vcc
.LBB0_508:
	v_max_f32_e32 v96, v49, v49
	v_max_f32_e32 v97, v48, v48
	v_max_f32_e32 v96, v97, v96
	v_max3_f32 v97, v50, v51, v33
	v_max3_f32 v96, v96, v32, v34
	v_max3_f32 v96, v96, v35, v52
	v_max3_f32 v97, v97, v54, v55
	v_max3_f32 v96, v96, v53, v36
	v_max3_f32 v97, v97, v38, v39
	v_max3_f32 v96, v96, v37, v56
	v_max3_f32 v97, v97, v58, v59
	v_max3_f32 v96, v96, v57, v40
	v_max3_f32 v97, v97, v42, v43
	v_max3_f32 v96, v96, v41, v60
	v_max3_f32 v97, v97, v62, v63
	v_max3_f32 v96, v96, v61, v44
	v_max3_f32 v97, v97, v46, v47
	v_max3_f32 v96, v96, v45, v97
	v_mov_b32_e32 v97, v96
	s_nop 1
	v_permlane32_swap_b32_e32 v96, v97
	v_max_f32_e32 v97, v97, v97
	v_max_f32_e32 v96, v96, v96
	v_max_f32_e32 v96, v96, v97
	v_cmp_lg_f32_e32 vcc, s23, v96
	s_xor_b64 s[0:1], s[44:45], -1
	s_and_b64 s[0:1], vcc, s[0:1]
	v_cmp_lt_f32_e32 vcc, s24, v96
	s_or_b64 s[6:7], vcc, s[0:1]
	v_cndmask_b32_e64 v97, 0, 1, s[6:7]
	v_cmp_ne_u32_e32 vcc, 0, v97
	s_cbranch_vccz .LBB0_512
	v_cndmask_b32_e64 v97, 0, v96, s[0:1]
	v_max_f32_e32 v96, v96, v96
	v_max_f32_e32 v96, 0, v96
	v_cndmask_b32_e64 v96, v97, v96, s[44:45]
	v_exp_f32_e64 v97, -v96
	s_nop 0
	v_cndmask_b32_e64 v97, v97, 1.0, s[0:1]
	s_and_saveexec_b64 s[0:1], s[4:5]
	ds_write_b32 v167, v97 offset:49152
	s_or_b64 exec, exec, s[0:1]
	s_waitcnt lgkmcnt(0)
	v_mul_f32_e32 v196, v196, v97
	v_add_f32_e64 v48, v48, -v96
	v_add_f32_e64 v49, v49, -v96
	v_add_f32_e64 v32, v32, -v96
	v_add_f32_e64 v33, v33, -v96
	v_add_f32_e64 v50, v50, -v96
	v_add_f32_e64 v51, v51, -v96
	v_add_f32_e64 v34, v34, -v96
	v_add_f32_e64 v35, v35, -v96
	v_add_f32_e64 v52, v52, -v96
	v_add_f32_e64 v53, v53, -v96
	v_add_f32_e64 v36, v36, -v96
	v_add_f32_e64 v37, v37, -v96
	v_add_f32_e64 v54, v54, -v96
	v_add_f32_e64 v55, v55, -v96
	v_add_f32_e64 v38, v38, -v96
	v_add_f32_e64 v39, v39, -v96
	v_add_f32_e64 v56, v56, -v96
	v_add_f32_e64 v57, v57, -v96
	v_add_f32_e64 v40, v40, -v96
	v_add_f32_e64 v41, v41, -v96
	v_add_f32_e64 v58, v58, -v96
	v_add_f32_e64 v59, v59, -v96
	v_add_f32_e64 v42, v42, -v96
	v_add_f32_e64 v43, v43, -v96
	v_add_f32_e64 v60, v60, -v96
	v_add_f32_e64 v61, v61, -v96
	v_add_f32_e64 v44, v44, -v96
	v_add_f32_e64 v45, v45, -v96
	v_add_f32_e64 v62, v62, -v96
	v_add_f32_e64 v63, v63, -v96
	v_add_f32_e64 v46, v46, -v96
	v_add_f32_e64 v47, v47, -v96
	ds_read_b128 v[96:99], v168 offset:49152
	ds_read_b128 v[100:103], v168 offset:49184
	ds_read_b128 v[104:107], v168 offset:49216
	ds_read_b128 v[108:111], v168 offset:49248
	s_waitcnt lgkmcnt(0)
	v_mul_f32_e32 v2, v2, v98
	v_mul_f32_e32 v3, v3, v99
	v_mul_f32_e32 v6, v6, v102
	v_mul_f32_e32 v7, v7, v103
	v_mul_f32_e32 v10, v10, v106
	v_mul_f32_e32 v11, v11, v107
	v_mul_f32_e32 v14, v14, v110
	v_mul_f32_e32 v15, v15, v111
	v_mul_f32_e32 v12, v12, v108
	v_mul_f32_e32 v13, v13, v109
	v_mul_f32_e32 v8, v8, v104
	v_mul_f32_e32 v9, v9, v105
	v_mul_f32_e32 v4, v4, v100
	v_mul_f32_e32 v5, v5, v101
	v_mul_f32_e32 v0, v0, v96
	v_mul_f32_e32 v1, v1, v97
	v_mul_f32_e32 v30, v30, v110
	v_mul_f32_e32 v31, v31, v111
	v_mul_f32_e32 v26, v26, v106
	v_mul_f32_e32 v27, v27, v107
	v_mul_f32_e32 v22, v22, v102
	v_mul_f32_e32 v23, v23, v103
	v_mul_f32_e32 v18, v18, v98
	v_mul_f32_e32 v19, v19, v99
	v_mul_f32_e32 v28, v28, v108
	v_mul_f32_e32 v29, v29, v109
	v_mul_f32_e32 v24, v24, v104
	v_mul_f32_e32 v25, v25, v105
	v_mul_f32_e32 v20, v20, v100
	v_mul_f32_e32 v21, v21, v101
	v_mul_f32_e32 v16, v16, v96
	v_mul_f32_e32 v17, v17, v97
.LBB0_512:
	v_exp_f32_e32 v97, v48
	v_exp_f32_e32 v96, v32
	v_exp_f32_e32 v49, v49
	v_exp_f32_e32 v48, v33
	v_exp_f32_e32 v99, v50
	v_exp_f32_e32 v98, v34
	v_exp_f32_e32 v51, v51
	v_exp_f32_e32 v50, v35
	v_exp_f32_e32 v103, v52
	v_exp_f32_e32 v53, v53
	v_exp_f32_e32 v105, v54
	v_exp_f32_e32 v55, v55
	v_cvt_pk_bf16_f32 v32, v97, v49
	v_cvt_pk_bf16_f32 v33, v99, v51
	v_cvt_pk_bf16_f32 v34, v103, v53
	v_cvt_pk_bf16_f32 v35, v105, v55
	v_add_f32_e32 v100, 0, v96
	v_add_f32_e32 v101, 0, v97
	v_mfma_f32_32x32x16_bf16 v[0:15], v[32:35], v[88:91], v[0:15]
	v_add_f32_e64 v88, v48, v100
	v_add_f32_e64 v89, v49, v101
	v_exp_f32_e32 v91, v56
	v_exp_f32_e32 v57, v57
	v_exp_f32_e32 v101, v58
	v_exp_f32_e32 v59, v59
	v_exp_f32_e32 v107, v60
	v_exp_f32_e32 v49, v61
	s_waitcnt lgkmcnt(0)
	v_mfma_f32_32x32x16_bf16 v[16:31], v[32:35], v[92:95], v[16:31]
	v_exp_f32_e32 v61, v62
	v_exp_f32_e32 v63, v63
	v_cvt_pk_bf16_f32 v32, v91, v57
	v_cvt_pk_bf16_f32 v33, v101, v59
	v_cvt_pk_bf16_f32 v34, v107, v49
	v_cvt_pk_bf16_f32 v35, v61, v63
	v_exp_f32_e32 v102, v36
	v_mfma_f32_32x32x16_bf16 v[0:15], v[32:35], v[84:87], v[0:15]
	v_exp_f32_e32 v52, v37
	v_add_f32_e32 v88, v98, v88
	v_add_f32_e32 v89, v99, v89
	v_exp_f32_e32 v104, v38
	v_exp_f32_e32 v54, v39
	v_add_f32_e32 v84, v50, v88
	v_add_f32_e32 v85, v51, v89
	v_exp_f32_e32 v90, v40
	v_add_f32_e32 v36, v102, v84
	v_add_f32_e32 v37, v103, v85
	v_mfma_f32_32x32x16_bf16 v[16:31], v[32:35], v[72:75], v[16:31]
	v_cvt_pk_bf16_f32 v32, v96, v48
	v_cvt_pk_bf16_f32 v33, v98, v50
	v_cvt_pk_bf16_f32 v34, v102, v52
	v_cvt_pk_bf16_f32 v35, v104, v54
	v_exp_f32_e32 v56, v41
	v_add_f32_e32 v36, v52, v36
	v_add_f32_e32 v37, v53, v37
	v_exp_f32_e32 v100, v42
	v_mfma_f32_32x32x16_bf16 v[0:15], v[32:35], v[80:83], v[0:15]
	v_add_f32_e64 v36, v104, v36
	v_add_f32_e64 v37, v105, v37
	v_exp_f32_e32 v58, v43
	v_add_f32_e32 v36, v54, v36
	v_add_f32_e32 v37, v55, v37
	v_exp_f32_e32 v106, v44
	v_exp_f32_e32 v48, v45
	v_exp_f32_e32 v60, v46
	v_exp_f32_e32 v62, v47
	v_mfma_f32_32x32x16_bf16 v[16:31], v[32:35], v[68:71], v[16:31]
	v_add_f32_e64 v32, v90, v36
	v_add_f32_e64 v33, v91, v37
	v_add_f32_e64 v32, v56, v32
	v_add_f32_e64 v33, v57, v33
	v_add_f32_e64 v36, v100, v32
	v_add_f32_e64 v37, v101, v33
	v_cvt_pk_bf16_f32 v32, v90, v56
	v_cvt_pk_bf16_f32 v33, v100, v58
	v_cvt_pk_bf16_f32 v34, v106, v48
	v_cvt_pk_bf16_f32 v35, v60, v62
	s_nop 0
	v_mfma_f32_32x32x16_bf16 v[0:15], v[32:35], v[76:79], v[0:15]
	v_add_f32_e64 v36, v58, v36
	v_add_f32_e64 v37, v59, v37
	v_add_f32_e64 v36, v106, v36
	v_add_f32_e64 v37, v107, v37
	v_add_f32_e64 v36, v48, v36
	v_add_f32_e64 v37, v49, v37
	v_add_f32_e32 v36, v60, v36
	v_add_f32_e32 v37, v61, v37
	v_mfma_f32_32x32x16_bf16 v[16:31], v[32:35], v[64:67], v[16:31]
	v_add_f32_e64 v36, v62, v36
	v_add_f32_e64 v37, v63, v37
	v_add_f32_e32 v36, v36, v37
	v_add_f32_e32 v196, v196, v36

.LBB0_1407:
	s_lshl_b32 s0, s46, 8
	s_lshl_b32 s41, s45, 6
	s_add_i32 s0, s0, s19
	s_cmp_lt_i32 s42, 0
	s_cbranch_scc1 .LBB0_1424
	s_add_i32 s45, s45, 1
	v_cvt_f32_ubyte0_e32 v1, s45
	v_mul_f32_e32 v2, -0.5, v1
	s_mov_b32 s45, 0xc2fc0000
	v_cmp_gt_f32_e32 vcc, s45, v2
	s_and_b64 s[46:47], vcc, exec
	s_cselect_b32 s48, 0xffffffc0, 0
	s_lshl_b32 s45, s41, 1
	s_add_u32 s46, s43, s45
	s_addc_u32 s47, s44, 0
	v_or_b32_e32 v5, s0, v155
	v_mov_b64_e32 v[2:3], s[46:47]
	v_mad_u64_u32 v[2:3], s[44:45], v5, s21, v[2:3]
	v_lshl_add_u64 v[2:3], v[118:119], 1, v[2:3]
	global_load_dwordx4 v[64:67], v[2:3], off offset:96
	global_load_dwordx4 v[68:71], v[2:3], off offset:64
	global_load_dwordx4 v[72:75], v[2:3], off offset:32
	global_load_dwordx4 v[76:79], v[2:3], off
	v_cndmask_b32_e32 v4, 0, v185, vcc
	v_fmac_f32_e32 v4, -0.5, v1
	v_exp_f32_e32 v1, v4
	s_waitcnt vmcnt(0)
	v_mul_f32_e32 v189, 0x3fb8aa3b, v0
	s_lshl_b32 s38, s38, 8
	v_mov_b32_e32 v14, v117
	v_ldexp_f32 v1, v1, s48
	v_mul_f32_e32 v135, 0x3fb8aa3b, v1
	s_lshl_b32 s48, s49, 6
	v_mov_b32_e32 v2, v135
	v_subrev_u32_e32 v0, s48, v163
	v_mov_b32_e32 v15, v117
	v_mul_f32_e32 v136, s14, v2
	v_mul_f32_e32 v137, s15, v2
	v_mul_f32_e32 v138, s16, v2
	v_mul_f32_e32 v139, s17, v2
	v_mul_f32_e32 v140, s24, v2
	v_mul_f32_e32 v141, s25, v2
	v_mul_f32_e32 v142, s26, v2
	v_mul_f32_e32 v143, s27, v2
	v_mul_f32_e32 v144, s30, v2
	v_mul_f32_e32 v145, s31, v2
	v_mul_f32_e32 v146, s34, v2
	v_mul_f32_e32 v147, s35, v2
	v_mul_f32_e32 v148, s36, v2
	v_mul_f32_e32 v149, s37, v2
	v_mul_f32_e32 v150, 0x42000000, v135
	s_sub_i32 s47, s39, s49
	v_subrev_u32_e32 v190, s38, v0
	s_add_i32 s38, s48, s38
	v_mov_b32_e32 v0, v117
	v_mov_b32_e32 v1, v117
	v_mov_b32_e32 v2, v117
	v_mov_b32_e32 v3, v117
	v_mov_b32_e32 v4, v117
	v_mov_b32_e32 v5, v117
	v_mov_b32_e32 v6, v117
	v_mov_b32_e32 v7, v117
	v_mov_b32_e32 v8, v117
	v_mov_b32_e32 v9, v117
	v_mov_b32_e32 v10, v117
	v_mov_b32_e32 v11, v117
	v_mov_b32_e32 v12, v117
	v_mov_b32_e32 v13, v117
	v_mov_b64_e32 v[30:31], v[14:15]
	s_mov_b32 s43, 0
	v_mul_f32_e32 v134, 0, v135
	s_or_b32 s44, s0, 31
	s_add_i32 s45, s0, 0xffffff81
	s_add_i32 s46, s0, 0xffffffa0
	s_add_i32 s47, s47, 4
	v_mov_b32_e32 v152, v150
	v_mov_b32_e32 v153, v150
	v_add_u32_e32 v191, s38, v164
	s_add_i32 s49, s49, 2
	s_movk_i32 s50, 0x4000
	v_mov_b64_e32 v[28:29], v[12:13]
	v_mov_b64_e32 v[26:27], v[10:11]
	v_mov_b64_e32 v[24:25], v[8:9]
	v_mov_b64_e32 v[22:23], v[6:7]
	v_mov_b64_e32 v[20:21], v[4:5]
	v_mov_b64_e32 v[18:19], v[2:3]
	v_mov_b64_e32 v[16:17], v[0:1]
	v_mov_b32_e32 v192, v156
	s_mov_b32 s52, 0
	s_mov_b32 s62, s64
	s_branch .LBB0_1412
.LBB0_1409:
	s_or_b64 exec, exec, s[38:39]
	s_waitcnt lgkmcnt(0)
	ds_read_b128 v[194:197], v160 offset:49152
	ds_read_b128 v[198:201], v160 offset:49184
	ds_read_b128 v[202:205], v160 offset:49216
	ds_read_b128 v[206:209], v160 offset:49248
	v_add_f32_e32 v189, v189, v154
	v_add_f32_e64 v48, v48, -v154
	v_add_f32_e64 v49, v49, -v154
	v_add_f32_e64 v32, v32, -v154
	v_add_f32_e64 v33, v33, -v154
	v_add_f32_e64 v50, v50, -v154
	v_add_f32_e64 v51, v51, -v154
	v_add_f32_e64 v34, v34, -v154
	v_add_f32_e64 v35, v35, -v154
	v_add_f32_e64 v52, v52, -v154
	v_add_f32_e64 v53, v53, -v154
	v_add_f32_e64 v36, v36, -v154
	v_add_f32_e64 v37, v37, -v154
	v_add_f32_e64 v54, v54, -v154
	v_add_f32_e64 v55, v55, -v154
	v_add_f32_e64 v38, v38, -v154
	v_add_f32_e64 v39, v39, -v154
	v_add_f32_e64 v56, v56, -v154
	v_add_f32_e64 v57, v57, -v154
	v_add_f32_e64 v40, v40, -v154
	v_add_f32_e64 v41, v41, -v154
	v_add_f32_e64 v58, v58, -v154
	v_add_f32_e64 v59, v59, -v154
	v_add_f32_e64 v42, v42, -v154
	v_add_f32_e64 v43, v43, -v154
	v_add_f32_e64 v60, v60, -v154
	v_add_f32_e64 v61, v61, -v154
	v_add_f32_e64 v44, v44, -v154
	v_add_f32_e64 v45, v45, -v154
	v_add_f32_e64 v62, v62, -v154
	v_add_f32_e64 v63, v63, -v154
	v_add_f32_e64 v46, v46, -v154
	v_add_f32_e64 v47, v47, -v154
	v_mul_f32_e32 v192, v192, v151
	s_waitcnt lgkmcnt(0)
	v_mul_f32_e32 v14, v14, v208
	v_mul_f32_e32 v15, v15, v209
	v_mul_f32_e32 v10, v10, v204
	v_mul_f32_e32 v11, v11, v205
	v_mul_f32_e32 v6, v6, v200
	v_mul_f32_e32 v7, v7, v201
	v_mul_f32_e32 v2, v2, v196
	v_mul_f32_e32 v3, v3, v197
	v_mul_f32_e32 v12, v12, v206
	v_mul_f32_e32 v13, v13, v207
	v_mul_f32_e32 v8, v8, v202
	v_mul_f32_e32 v9, v9, v203
	v_mul_f32_e32 v4, v4, v198
	v_mul_f32_e32 v5, v5, v199
	v_mul_f32_e32 v0, v0, v194
	v_mul_f32_e32 v1, v1, v195
	v_mul_f32_e32 v30, v30, v208
	v_mul_f32_e32 v31, v31, v209
	v_mul_f32_e32 v26, v26, v204
	v_mul_f32_e32 v27, v27, v205
	v_mul_f32_e32 v22, v22, v200
	v_mul_f32_e32 v23, v23, v201
	v_mul_f32_e32 v18, v18, v196
	v_mul_f32_e32 v19, v19, v197
	v_mul_f32_e32 v28, v28, v206
	v_mul_f32_e32 v29, v29, v207
	v_mul_f32_e32 v24, v24, v202
	v_mul_f32_e32 v25, v25, v203
	v_mul_f32_e32 v20, v20, v198
	v_mul_f32_e32 v21, v21, v199
	v_mul_f32_e32 v16, v16, v194
	v_mul_f32_e32 v17, v17, v195
.LBB0_1410:
	v_exp_f32_e32 v195, v48
	v_exp_f32_e32 v194, v32
	v_exp_f32_e32 v49, v49
	v_exp_f32_e32 v48, v33
	v_exp_f32_e32 v197, v50
	v_exp_f32_e32 v196, v34
	v_exp_f32_e32 v51, v51
	v_exp_f32_e32 v50, v35
	v_exp_f32_e32 v201, v52
	v_exp_f32_e32 v53, v53
	v_exp_f32_e32 v203, v54
	v_exp_f32_e32 v55, v55
	v_cvt_pk_bf16_f32 v32, v195, v49
	v_cvt_pk_bf16_f32 v33, v197, v51
	v_cvt_pk_bf16_f32 v34, v201, v53
	v_cvt_pk_bf16_f32 v35, v203, v55
	v_add_f32_e32 v198, 0, v194
	v_add_f32_e32 v199, 0, v195
	v_mfma_f32_32x32x16_bf16 v[0:15], v[32:35], v[100:103], v[0:15]
	v_add_f32_e64 v100, v48, v198
	v_add_f32_e64 v101, v49, v199
	v_exp_f32_e32 v103, v56
	v_exp_f32_e32 v57, v57
	v_exp_f32_e32 v199, v58
	v_exp_f32_e32 v59, v59
	v_exp_f32_e32 v205, v60
	v_exp_f32_e32 v49, v61
	s_waitcnt lgkmcnt(0)
	v_mfma_f32_32x32x16_bf16 v[16:31], v[32:35], v[108:111], v[16:31]
	v_exp_f32_e32 v61, v62
	v_exp_f32_e32 v63, v63
	v_cvt_pk_bf16_f32 v32, v103, v57
	v_cvt_pk_bf16_f32 v33, v199, v59
	v_cvt_pk_bf16_f32 v34, v205, v49
	v_cvt_pk_bf16_f32 v35, v61, v63
	v_exp_f32_e32 v200, v36
	v_mfma_f32_32x32x16_bf16 v[0:15], v[32:35], v[92:95], v[0:15]
	v_exp_f32_e32 v52, v37
	v_add_f32_e32 v100, v196, v100
	v_add_f32_e32 v101, v197, v101
	v_exp_f32_e32 v202, v38
	v_exp_f32_e32 v54, v39
	v_add_f32_e32 v92, v50, v100
	v_add_f32_e32 v93, v51, v101
	v_exp_f32_e32 v102, v40
	v_add_f32_e32 v36, v200, v92
	v_add_f32_e32 v37, v201, v93
	v_mfma_f32_32x32x16_bf16 v[16:31], v[32:35], v[104:107], v[16:31]
	v_cvt_pk_bf16_f32 v32, v194, v48
	v_cvt_pk_bf16_f32 v33, v196, v50
	v_cvt_pk_bf16_f32 v34, v200, v52
	v_cvt_pk_bf16_f32 v35, v202, v54
	v_exp_f32_e32 v56, v41
	v_add_f32_e32 v36, v52, v36
	v_add_f32_e32 v37, v53, v37
	v_exp_f32_e32 v198, v42
	v_mfma_f32_32x32x16_bf16 v[0:15], v[32:35], v[84:87], v[0:15]
	v_add_f32_e64 v36, v202, v36
	v_add_f32_e64 v37, v203, v37
	v_exp_f32_e32 v58, v43
	v_add_f32_e32 v36, v54, v36
	v_add_f32_e32 v37, v55, v37
	v_exp_f32_e32 v204, v44
	v_exp_f32_e32 v48, v45
	v_exp_f32_e32 v60, v46
	v_exp_f32_e32 v62, v47
	v_mfma_f32_32x32x16_bf16 v[16:31], v[32:35], v[96:99], v[16:31]
	v_add_f32_e64 v32, v102, v36
	v_add_f32_e64 v33, v103, v37
	v_add_f32_e64 v32, v56, v32
	v_add_f32_e64 v33, v57, v33
	v_add_f32_e64 v36, v198, v32
	v_add_f32_e64 v37, v199, v33
	v_cvt_pk_bf16_f32 v32, v102, v56
	v_cvt_pk_bf16_f32 v33, v198, v58
	v_cvt_pk_bf16_f32 v34, v204, v48
	v_cvt_pk_bf16_f32 v35, v60, v62
	s_nop 0
	v_mfma_f32_32x32x16_bf16 v[0:15], v[32:35], v[80:83], v[0:15]
	v_add_f32_e64 v36, v58, v36
	v_add_f32_e64 v37, v59, v37
	v_add_f32_e64 v36, v204, v36
	v_add_f32_e64 v37, v205, v37
	v_add_f32_e64 v36, v48, v36
	v_add_f32_e64 v37, v49, v37
	v_add_f32_e32 v36, v60, v36
	v_add_f32_e32 v37, v61, v37
	v_mfma_f32_32x32x16_bf16 v[16:31], v[32:35], v[88:91], v[16:31]
	v_add_f32_e64 v36, v62, v36
	v_add_f32_e64 v37, v63, v37
	v_add_f32_e32 v36, v36, v37
	v_add_f32_e32 v192, v192, v36

.LBB0_1418:
	s_cmp_le_i32 s48, s44
	s_cselect_b64 s[52:53], -1, 0
	s_add_i32 s38, s48, 63
	s_cmp_ge_i32 s38, s45
	s_cselect_b64 s[54:55], -1, 0
	s_and_b64 s[52:53], s[52:53], s[54:55]
	s_andn2_b64 vcc, exec, s[52:53]
	s_cbranch_vccnz .LBB0_1411
	v_add_u32_e32 v154, s43, v157
	v_cvt_f32_i32_e32 v32, v191
	ds_read_b128 v[80:83], v154
	ds_read_b128 v[84:87], v154 offset:512
	ds_read_b128 v[88:91], v154 offset:2048
	ds_read_b128 v[96:99], v154 offset:2560
	v_mov_b32_e32 v151, v150
	v_fma_f32 v32, v135, v32, -v189
	v_add_f32_e32 v48, v134, v32
	v_add_f32_e32 v49, v135, v32
	v_add_f32_e32 v50, v136, v32
	v_add_f32_e32 v51, v137, v32
	v_add_f32_e32 v52, v138, v32
	v_add_f32_e32 v53, v139, v32
	v_add_f32_e32 v54, v140, v32
	v_add_f32_e32 v55, v141, v32
	v_add_f32_e32 v56, v142, v32
	v_add_f32_e32 v57, v143, v32
	v_add_f32_e32 v58, v144, v32
	v_add_f32_e32 v59, v145, v32
	v_add_f32_e32 v60, v146, v32
	v_add_f32_e32 v61, v147, v32
	v_add_f32_e32 v62, v148, v32
	v_add_f32_e32 v63, v149, v32
	v_add_f32_e32 v44, v150, v60
	v_add_f32_e32 v45, v151, v61
	v_add_f32_e32 v46, v150, v62
	v_add_f32_e32 v47, v151, v63
	v_add_f32_e32 v42, v150, v58
	v_add_f32_e32 v43, v151, v59
	v_add_f32_e32 v40, v150, v56
	v_add_f32_e32 v41, v151, v57
	v_add_f32_e32 v38, v150, v54
	v_add_f32_e32 v39, v151, v55
	v_add_f32_e32 v36, v150, v52
	v_add_f32_e32 v37, v151, v53
	v_add_f32_e32 v34, v150, v50
	v_add_f32_e32 v35, v151, v51
	v_add_f32_e32 v32, v152, v48
	v_add_f32_e32 v33, v153, v49
	v_add_u32_e32 v151, s43, v158
	ds_read_b64_tr_b16 v[100:101], v151 offset:24576
	ds_read_b64_tr_b16 v[102:103], v151 offset:25088
	ds_read_b64_tr_b16 v[92:93], v151 offset:25600
	ds_read_b64_tr_b16 v[94:95], v151 offset:26112
	ds_read_b128 v[104:107], v154 offset:4096
	ds_read_b128 v[108:111], v154 offset:4608
	s_waitcnt lgkmcnt(0)
	v_mfma_f32_32x32x16_bf16 v[48:63], v[80:83], v[76:79], v[48:63]
	v_mfma_f32_32x32x16_bf16 v[32:47], v[84:87], v[76:79], v[32:47]
	ds_read_b64_tr_b16 v[84:85], v151 offset:26624
	ds_read_b64_tr_b16 v[86:87], v151 offset:27136
	ds_read_b64_tr_b16 v[80:81], v151 offset:27648
	ds_read_b64_tr_b16 v[82:83], v151 offset:28160
	ds_read_b128 v[194:197], v154 offset:6144
	ds_read_b128 v[198:201], v154 offset:6656
	v_mfma_f32_32x32x16_bf16 v[48:63], v[88:91], v[72:75], v[48:63]
	v_mfma_f32_32x32x16_bf16 v[32:47], v[96:99], v[72:75], v[32:47]
	v_mfma_f32_32x32x16_bf16 v[48:63], v[104:107], v[68:71], v[48:63]
	v_mfma_f32_32x32x16_bf16 v[32:47], v[108:111], v[68:71], v[32:47]
	s_waitcnt lgkmcnt(0)
	v_mfma_f32_32x32x16_bf16 v[48:63], v[194:197], v[64:67], v[48:63]
	ds_read_b64_tr_b16 v[108:109], v151 offset:28672
	ds_read_b64_tr_b16 v[110:111], v151 offset:29184
	ds_read_b64_tr_b16 v[104:105], v151 offset:29696
	ds_read_b64_tr_b16 v[106:107], v151 offset:30208
	v_mfma_f32_32x32x16_bf16 v[32:47], v[198:201], v[64:67], v[32:47]
	ds_read_b64_tr_b16 v[96:97], v151 offset:30720
	ds_read_b64_tr_b16 v[98:99], v151 offset:31232
	ds_read_b64_tr_b16 v[88:89], v151 offset:31744
	ds_read_b64_tr_b16 v[90:91], v151 offset:32256
	s_cmp_lt_i32 s48, s46
	s_cselect_b64 s[52:53], -1, 0
	s_cmp_gt_i32 s38, s0
	s_cselect_b64 s[38:39], -1, 0
	s_or_b64 s[38:39], s[52:53], s[38:39]
	s_andn2_b64 vcc, exec, s[38:39]
	s_cbranch_vccnz .LBB0_1421
	v_add_u32_e32 v151, 59, v190
	v_add_u32_e32 v154, 27, v190
	v_cmp_gt_u32_e32 vcc, s22, v151
	v_add_u32_e32 v151, 58, v190
	s_nop 0
	v_cndmask_b32_e32 v48, v186, v48, vcc
	v_cmp_gt_u32_e32 vcc, s22, v154
	v_add_u32_e32 v154, 26, v190
	s_nop 0
	v_cndmask_b32_e32 v32, v186, v32, vcc
	v_cmp_gt_u32_e32 vcc, s22, v151
	v_add_u32_e32 v151, 57, v190
	s_nop 0
	v_cndmask_b32_e32 v49, v186, v49, vcc
	v_cmp_gt_u32_e32 vcc, s22, v154
	v_add_u32_e32 v154, 25, v190
	s_nop 0
	v_cndmask_b32_e32 v33, v186, v33, vcc
	v_cmp_gt_u32_e32 vcc, s22, v151
	v_add_u32_e32 v151, 56, v190
	s_nop 0
	v_cndmask_b32_e32 v50, v186, v50, vcc
	v_cmp_gt_u32_e32 vcc, s22, v154
	v_add_u32_e32 v154, 24, v190
	s_nop 0
	v_cndmask_b32_e32 v34, v186, v34, vcc
	v_cmp_gt_u32_e32 vcc, s22, v151
	v_add_u32_e32 v151, 51, v190
	s_nop 0
	v_cndmask_b32_e32 v51, v186, v51, vcc
	v_cmp_gt_u32_e32 vcc, s22, v154
	v_add_u32_e32 v154, 19, v190
	s_nop 0
	v_cndmask_b32_e32 v35, v186, v35, vcc
	v_cmp_gt_u32_e32 vcc, s22, v151
	v_add_u32_e32 v151, 50, v190
	s_nop 0
	v_cndmask_b32_e32 v52, v186, v52, vcc
	v_cmp_gt_u32_e32 vcc, s22, v154
	v_add_u32_e32 v154, 18, v190
	s_nop 0
	v_cndmask_b32_e32 v36, v186, v36, vcc
	v_cmp_gt_u32_e32 vcc, s22, v151
	v_add_u32_e32 v151, 49, v190
	s_nop 0
	v_cndmask_b32_e32 v53, v186, v53, vcc
	v_cmp_gt_u32_e32 vcc, s22, v154
	v_add_u32_e32 v154, 17, v190
	s_nop 0
	v_cndmask_b32_e32 v37, v186, v37, vcc
	v_cmp_gt_u32_e32 vcc, s22, v151
	v_add_u32_e32 v151, 48, v190
	s_nop 0
	v_cndmask_b32_e32 v54, v186, v54, vcc
	v_cmp_gt_u32_e32 vcc, s22, v154
	v_add_u32_e32 v154, 16, v190
	s_nop 0
	v_cndmask_b32_e32 v38, v186, v38, vcc
	v_cmp_gt_u32_e32 vcc, s22, v151
	v_add_u32_e32 v151, 43, v190
	s_nop 0
	v_cndmask_b32_e32 v55, v186, v55, vcc
	v_cmp_gt_u32_e32 vcc, s22, v154
	v_add_u32_e32 v154, 11, v190
	s_nop 0
	v_cndmask_b32_e32 v39, v186, v39, vcc
	v_cmp_gt_u32_e32 vcc, s22, v151
	v_add_u32_e32 v151, 42, v190
	s_nop 0
	v_cndmask_b32_e32 v56, v186, v56, vcc
	v_cmp_gt_u32_e32 vcc, s22, v154
	v_add_u32_e32 v154, 10, v190
	s_nop 0
	v_cndmask_b32_e32 v40, v186, v40, vcc
	v_cmp_gt_u32_e32 vcc, s22, v151
	v_add_u32_e32 v151, 41, v190
	s_nop 0
	v_cndmask_b32_e32 v57, v186, v57, vcc
	v_cmp_gt_u32_e32 vcc, s22, v154
	v_add_u32_e32 v154, 9, v190
	s_nop 0
	v_cndmask_b32_e32 v41, v186, v41, vcc
	v_cmp_gt_u32_e32 vcc, s22, v151
	v_add_u32_e32 v151, 40, v190
	s_nop 0
	v_cndmask_b32_e32 v58, v186, v58, vcc
	v_cmp_gt_u32_e32 vcc, s22, v154
	v_add_u32_e32 v154, 8, v190
	s_nop 0
	v_cndmask_b32_e32 v42, v186, v42, vcc
	v_cmp_gt_u32_e32 vcc, s22, v151
	v_add_u32_e32 v151, 35, v190
	s_nop 0
	v_cndmask_b32_e32 v59, v186, v59, vcc
	v_cmp_gt_u32_e32 vcc, s22, v154
	v_add_u32_e32 v154, 3, v190
	s_nop 0
	v_cndmask_b32_e32 v43, v186, v43, vcc
	v_cmp_gt_u32_e32 vcc, s22, v151
	v_add_u32_e32 v151, 34, v190
	s_nop 0
	v_cndmask_b32_e32 v60, v186, v60, vcc
	v_cmp_gt_u32_e32 vcc, s22, v154
	v_add_u32_e32 v154, 2, v190
	s_nop 0
	v_cndmask_b32_e32 v44, v186, v44, vcc
	v_cmp_gt_u32_e32 vcc, s22, v151
	v_add_u32_e32 v151, 33, v190
	s_nop 0
	v_cndmask_b32_e32 v61, v186, v61, vcc
	v_cmp_gt_u32_e32 vcc, s22, v154
	v_add_u32_e32 v154, 1, v190
	s_nop 0
	v_cndmask_b32_e32 v45, v186, v45, vcc
	v_cmp_gt_u32_e32 vcc, s22, v151
	v_add_u32_e32 v151, 32, v190
	s_nop 0
	v_cndmask_b32_e32 v62, v186, v62, vcc
	v_cmp_gt_u32_e32 vcc, s22, v154
	s_nop 1
	v_cndmask_b32_e32 v46, v186, v46, vcc
	v_cmp_gt_u32_e32 vcc, s22, v151
	s_nop 1
	v_cndmask_b32_e32 v63, v186, v63, vcc
	v_cmp_gt_u32_e32 vcc, s22, v190
	s_nop 1
	v_cndmask_b32_e32 v47, v186, v47, vcc

.LBB0_3023:
	s_add_i32 s57, s57, 1
	v_cvt_f32_ubyte0_e32 v2, s57
	v_mul_f32_e32 v3, -0.5, v2
	s_mov_b32 s56, 0xc2fc0000
	v_cmp_gt_f32_e32 vcc, s56, v3
	s_and_b64 s[58:59], vcc, exec
	s_cselect_b32 s57, 0xffffffc0, 0
	v_cndmask_b32_e32 v3, 0, v191, vcc
	v_fmac_f32_e32 v3, -0.5, v2
	v_exp_f32_e32 v2, v3
	v_cmp_nlg_f32_e32 vcc, s48, v1
	s_or_b64 vcc, s[0:1], vcc
	v_mov_b32_e32 v14, v117
	v_cndmask_b32_e32 v3, v1, v192, vcc
	v_cmp_gt_f32_e64 s[0:1], v0, v3
	v_ldexp_f32 v2, v2, s57
	s_and_b64 s[0:1], s[6:7], s[0:1]
	v_mul_f32_e32 v137, 0x3fb8aa3b, v2
	v_cndmask_b32_e64 v2, 0, -1, vcc
	v_cndmask_b32_e64 v3, v3, v0, s[0:1]
	v_cndmask_b32_e64 v2, v2, 1, s[0:1]
	v_cmp_gt_f32_e64 s[0:1], v27, v3
	s_and_b64 s[0:1], s[30:31], s[0:1]
	s_lshl_b32 s57, s52, 2
	v_cndmask_b32_e64 v3, v3, v27, s[0:1]
	v_cndmask_b32_e64 v2, v2, 2, s[0:1]
	v_cmp_gt_f32_e64 s[0:1], v26, v3
	s_and_b64 s[0:1], s[34:35], s[0:1]
	s_add_i32 s57, s57, 4
	v_cndmask_b32_e64 v3, v3, v26, s[0:1]
	v_cndmask_b32_e64 v2, v2, 3, s[0:1]
	v_cmp_gt_f32_e64 s[0:1], v37, v3
	s_and_b64 s[0:1], s[36:37], s[0:1]
	v_mov_b32_e32 v15, v117
	v_cndmask_b32_e64 v3, v3, v37, s[0:1]
	v_cndmask_b32_e64 v2, v2, 4, s[0:1]
	v_cmp_gt_f32_e64 s[0:1], v36, v3
	s_and_b64 s[0:1], s[38:39], s[0:1]
	v_mul_f32_e32 v138, 0x42000000, v137
	v_cndmask_b32_e64 v3, v3, v36, s[0:1]
	v_cndmask_b32_e64 v2, v2, 5, s[0:1]
	v_cmp_gt_f32_e64 s[0:1], v38, v3
	s_and_b64 s[0:1], s[40:41], s[0:1]
	v_mov_b32_e32 v7, v117
	v_cndmask_b32_e64 v2, v2, 6, s[0:1]
	v_lshlrev_b32_e64 v3, v2, 1
	v_cmp_lt_i32_e64 s[0:1], -1, v2
	v_mov_b32_e32 v8, v117
	v_mov_b32_e32 v9, v117
	v_cndmask_b32_e64 v2, 0, v3, s[0:1]
	v_and_b32_e32 v3, 1, v2
	v_cmp_eq_u32_e64 s[0:1], 1, v3
	s_or_b64 s[0:1], vcc, s[0:1]
	v_and_b32_e32 v5, 2, v2
	v_cndmask_b32_e64 v3, 0, -1, s[0:1]
	v_cndmask_b32_e64 v4, v1, v192, s[0:1]
	v_cmp_eq_u32_e64 s[0:1], 0, v5
	s_and_b64 s[58:59], s[6:7], s[0:1]
	v_cmp_gt_f32_e64 s[0:1], v0, v4
	s_and_b64 s[0:1], s[58:59], s[0:1]
	v_and_b32_e32 v5, 4, v2
	v_cndmask_b32_e64 v3, v3, 1, s[0:1]
	v_cndmask_b32_e64 v4, v4, v0, s[0:1]
	v_cmp_eq_u32_e64 s[0:1], 0, v5
	s_and_b64 s[58:59], s[30:31], s[0:1]
	v_cmp_gt_f32_e64 s[0:1], v27, v4
	s_and_b64 s[0:1], s[58:59], s[0:1]
	v_and_b32_e32 v5, 8, v2
	v_cndmask_b32_e64 v3, v3, 2, s[0:1]
	v_cndmask_b32_e64 v4, v4, v27, s[0:1]
	v_cmp_eq_u32_e64 s[0:1], 0, v5
	s_and_b64 s[58:59], s[34:35], s[0:1]
	v_cmp_gt_f32_e64 s[0:1], v26, v4
	s_and_b64 s[0:1], s[58:59], s[0:1]
	v_and_b32_e32 v5, 16, v2
	v_cndmask_b32_e64 v3, v3, 3, s[0:1]
	v_cndmask_b32_e64 v4, v4, v26, s[0:1]
	v_cmp_eq_u32_e64 s[0:1], 0, v5
	s_and_b64 s[58:59], s[36:37], s[0:1]
	v_cmp_gt_f32_e64 s[0:1], v37, v4
	s_and_b64 s[0:1], s[58:59], s[0:1]
	v_and_b32_e32 v5, 32, v2
	v_cndmask_b32_e64 v3, v3, 4, s[0:1]
	v_cndmask_b32_e64 v4, v4, v37, s[0:1]
	v_cmp_eq_u32_e64 s[0:1], 0, v5
	s_and_b64 s[58:59], s[38:39], s[0:1]
	v_cmp_gt_f32_e64 s[0:1], v36, v4
	s_and_b64 s[0:1], s[58:59], s[0:1]
	v_and_b32_e32 v5, 64, v2
	v_cndmask_b32_e64 v3, v3, 5, s[0:1]
	v_cndmask_b32_e64 v4, v4, v36, s[0:1]
	v_cmp_eq_u32_e64 s[0:1], 0, v5
	s_and_b64 s[58:59], s[40:41], s[0:1]
	v_cmp_gt_f32_e64 s[0:1], v38, v4
	s_and_b64 s[0:1], s[58:59], s[0:1]
	v_mov_b32_e32 v10, v117
	v_cndmask_b32_e64 v3, v3, 6, s[0:1]
	v_lshlrev_b32_e64 v4, v3, 1
	v_cmp_lt_i32_e64 s[0:1], -1, v3
	v_mov_b32_e32 v11, v117
	v_mov_b32_e32 v12, v117
	v_cndmask_b32_e64 v3, 0, v4, s[0:1]
	v_or_b32_e32 v4, v3, v2
	v_and_b32_e32 v5, 1, v4
	v_cmp_eq_u32_e64 s[0:1], 1, v5
	s_or_b64 vcc, vcc, s[0:1]
	v_bitop3_b32 v6, v3, 2, v2 bitop3:0xc8
	v_cndmask_b32_e64 v5, 0, -1, vcc
	v_cndmask_b32_e32 v1, v1, v192, vcc
	v_cmp_eq_u32_e32 vcc, 0, v6
	s_and_b64 s[0:1], s[6:7], vcc
	v_cmp_gt_f32_e32 vcc, v0, v1
	s_and_b64 vcc, s[0:1], vcc
	v_mov_b32_e32 v6, v117
	v_cndmask_b32_e32 v0, v1, v0, vcc
	v_bitop3_b32 v1, v3, 4, v2 bitop3:0xc8
	v_cndmask_b32_e64 v5, v5, 1, vcc
	v_cmp_eq_u32_e32 vcc, 0, v1
	s_and_b64 s[0:1], s[30:31], vcc
	v_cmp_gt_f32_e32 vcc, v27, v0
	s_and_b64 vcc, s[0:1], vcc
	v_mov_b32_e32 v13, v117
	v_cndmask_b32_e64 v1, v5, 2, vcc
	v_bitop3_b32 v5, v3, 8, v2 bitop3:0xc8
	v_cndmask_b32_e32 v0, v0, v27, vcc
	v_cmp_eq_u32_e32 vcc, 0, v5
	s_and_b64 s[0:1], s[34:35], vcc
	v_cmp_gt_f32_e32 vcc, v26, v0
	s_and_b64 vcc, s[0:1], vcc
	v_bitop3_b32 v5, v3, 16, v2 bitop3:0xc8
	v_cndmask_b32_e64 v1, v1, 3, vcc
	v_cndmask_b32_e32 v0, v0, v26, vcc
	v_cmp_eq_u32_e32 vcc, 0, v5
	s_and_b64 s[0:1], s[36:37], vcc
	v_cmp_gt_f32_e32 vcc, v37, v0
	s_and_b64 vcc, s[0:1], vcc
	v_bitop3_b32 v5, v3, 32, v2 bitop3:0xc8
	v_cndmask_b32_e64 v1, v1, 4, vcc
	v_cndmask_b32_e32 v0, v0, v37, vcc
	v_cmp_eq_u32_e32 vcc, 0, v5
	s_and_b64 s[0:1], s[38:39], vcc
	v_cmp_gt_f32_e32 vcc, v36, v0
	s_and_b64 vcc, s[0:1], vcc
	v_bitop3_b32 v2, v3, 64, v2 bitop3:0xc8
	v_cndmask_b32_e64 v1, v1, 5, vcc
	v_cndmask_b32_e32 v0, v0, v36, vcc
	v_cmp_eq_u32_e32 vcc, 0, v2
	s_and_b64 s[0:1], s[40:41], vcc
	v_cmp_gt_f32_e32 vcc, v38, v0
	s_and_b64 s[0:1], s[0:1], vcc
	v_cndmask_b32_e64 v0, v1, 6, s[0:1]
	v_lshlrev_b32_e64 v1, v0, 1
	v_cmp_lt_i32_e32 vcc, -1, v0
	s_lshl_b32 s0, s53, 2
	s_or_b32 s37, s8, 31
	v_cndmask_b32_e32 v0, 0, v1, vcc
	s_sub_i32 s38, 31, s0
	s_lshl_b32 s0, s53, 8
	v_or_b32_e32 v198, v0, v4
	v_mov_b32_e32 v0, v137
	v_subrev_u32_e32 v200, s0, v171
	s_add_u32 s0, s54, s55
	v_mul_f32_e32 v142, s14, v0
	v_mul_f32_e32 v143, s15, v0
	v_mul_f32_e32 v144, s16, v0
	v_mul_f32_e32 v145, s17, v0
	v_mul_f32_e32 v146, s18, v0
	v_mul_f32_e32 v147, s19, v0
	v_mul_f32_e32 v148, s20, v0
	v_mul_f32_e32 v149, s21, v0
	v_mul_f32_e32 v150, s22, v0
	v_mul_f32_e32 v151, s23, v0
	v_mul_f32_e32 v152, s24, v0
	v_mul_f32_e32 v153, s25, v0
	v_mul_f32_e32 v154, s26, v0
	v_mul_f32_e32 v155, s27, v0
	s_addc_u32 s1, 0, 0
	v_mov_b32_e32 v0, v117
	v_mov_b32_e32 v1, v117
	v_mov_b32_e32 v2, v117
	v_mov_b32_e32 v3, v117
	v_mov_b32_e32 v4, v117
	v_mov_b32_e32 v5, v117
	v_mov_b64_e32 v[30:31], v[14:15]
	s_mov_b32 s56, 0
	v_mul_f32_e32 v136, 0, v137
	v_sub_u32_e32 v199, v164, v195
	v_mov_b32_e32 v140, v138
	v_mov_b32_e32 v141, v138
	v_lshl_add_u64 v[156:157], v[132:133], 0, s[0:1]
	v_lshl_add_u64 v[158:159], v[134:135], 0, s[0:1]
	s_movk_i32 s39, 0x4000
	s_mov_b64 s[30:31], 0
	v_mov_b64_e32 v[28:29], v[12:13]
	v_mov_b64_e32 v[26:27], v[10:11]
	v_mov_b64_e32 v[24:25], v[8:9]
	v_mov_b64_e32 v[22:23], v[6:7]
	v_mov_b64_e32 v[20:21], v[4:5]
	v_mov_b64_e32 v[18:19], v[2:3]
	v_mov_b64_e32 v[16:17], v[0:1]
	v_mov_b32_e32 v196, 0
	s_mov_b32 s36, 0
	s_mov_b32 s40, 0
	s_branch .LBB0_3026

.Lmoba1_a:
	v_and_b32_e32 v33, s6, v198
	v_cmp_ne_u32_e32 vcc, 0, v33
	v_fma_f32 v32, v137, v32, -v197
	s_or_b64 vcc, s[0:1], vcc
	v_cndmask_b32_e32 v32, v192, v32, vcc
	v_add_f32_e32 v48, v136, v32
	v_add_f32_e32 v49, v137, v32
	v_add_f32_e32 v50, v142, v32
	v_add_f32_e32 v51, v143, v32
	v_add_f32_e32 v52, v144, v32
	v_add_f32_e32 v53, v145, v32
	v_add_f32_e32 v54, v146, v32
	v_add_f32_e32 v55, v147, v32
	v_add_f32_e32 v56, v148, v32
	v_add_f32_e32 v57, v149, v32
	v_add_f32_e32 v58, v150, v32
	v_add_f32_e32 v59, v151, v32
	v_add_f32_e32 v60, v152, v32
	v_add_f32_e32 v61, v153, v32
	v_add_f32_e32 v62, v154, v32
	v_add_f32_e32 v63, v155, v32
	v_mov_b32_e32 v139, v138
	v_add_f32_e32 v46, v138, v62
	v_add_f32_e32 v47, v139, v63
	v_add_f32_e32 v44, v138, v60
	v_add_f32_e32 v45, v139, v61
	v_add_f32_e32 v42, v138, v58
	v_add_f32_e32 v43, v139, v59
	v_add_f32_e32 v40, v138, v56
	v_add_f32_e32 v41, v139, v57
	v_add_f32_e32 v38, v138, v54
	v_add_f32_e32 v39, v139, v55
	v_add_f32_e32 v36, v138, v52
	v_add_f32_e32 v37, v139, v53
	v_add_f32_e32 v34, v138, v50
	v_add_f32_e32 v35, v139, v51
	v_add_f32_e32 v32, v140, v48
	v_add_f32_e32 v33, v141, v49
	v_add_u32_e32 v139, s36, v166
	ds_read_b64_tr_b16 v[100:101], v139 offset:24576
	ds_read_b64_tr_b16 v[102:103], v139 offset:25088
	ds_read_b64_tr_b16 v[92:93], v139 offset:25600
	ds_read_b64_tr_b16 v[94:95], v139 offset:26112
	ds_read_b128 v[108:111], v160 offset:4096
	ds_read_b128 v[202:205], v160 offset:4608
	s_waitcnt lgkmcnt(0)
	v_mfma_f32_32x32x16_bf16 v[48:63], v[80:83], v[76:79], v[48:63]
	ds_read_b64_tr_b16 v[84:85], v139 offset:26624
	ds_read_b64_tr_b16 v[86:87], v139 offset:27136
	ds_read_b64_tr_b16 v[80:81], v139 offset:27648
	ds_read_b64_tr_b16 v[82:83], v139 offset:28160
	ds_read_b128 v[206:209], v160 offset:6144
	ds_read_b128 v[210:213], v160 offset:6656
	v_mfma_f32_32x32x16_bf16 v[32:47], v[88:91], v[76:79], v[32:47]
	v_mfma_f32_32x32x16_bf16 v[48:63], v[96:99], v[72:75], v[48:63]
	v_mfma_f32_32x32x16_bf16 v[32:47], v[104:107], v[72:75], v[32:47]
	v_mfma_f32_32x32x16_bf16 v[48:63], v[108:111], v[68:71], v[48:63]
	v_mfma_f32_32x32x16_bf16 v[32:47], v[202:205], v[68:71], v[32:47]
	s_waitcnt lgkmcnt(0)
	v_mfma_f32_32x32x16_bf16 v[48:63], v[206:209], v[64:67], v[48:63]
	ds_read_b64_tr_b16 v[108:109], v139 offset:28672
	ds_read_b64_tr_b16 v[110:111], v139 offset:29184
	ds_read_b64_tr_b16 v[104:105], v139 offset:29696
	ds_read_b64_tr_b16 v[106:107], v139 offset:30208
	v_mfma_f32_32x32x16_bf16 v[32:47], v[210:213], v[64:67], v[32:47]
	ds_read_b64_tr_b16 v[96:97], v139 offset:30720
	ds_read_b64_tr_b16 v[98:99], v139 offset:31232
	ds_read_b64_tr_b16 v[88:89], v139 offset:31744
	ds_read_b64_tr_b16 v[90:91], v139 offset:32256
	s_add_i32 s6, s56, 63
	s_cmp_gt_u32 s6, s8
	s_cselect_b64 s[6:7], -1, 0
	s_and_b64 s[0:1], s[0:1], s[6:7]
	s_andn2_b64 vcc, exec, s[0:1]
	s_cbranch_vccnz .LBB0_3035
	v_add_u32_e32 v139, 27, v200
	v_cmp_lt_i32_e32 vcc, -1, v139
	s_nop 1
	v_cndmask_b32_e32 v48, v192, v48, vcc
	v_cmp_lt_i32_e32 vcc, 31, v139
	v_add_u32_e32 v139, 26, v200
	s_nop 0
	v_cndmask_b32_e32 v32, v192, v32, vcc
	v_cmp_lt_i32_e32 vcc, -1, v139
	s_nop 1
	v_cndmask_b32_e32 v49, v192, v49, vcc
	v_cmp_lt_i32_e32 vcc, 31, v139
	v_add_u32_e32 v139, 25, v200
	s_nop 0
	v_cndmask_b32_e32 v33, v192, v33, vcc
	v_cmp_lt_i32_e32 vcc, -1, v139
	s_nop 1
	v_cndmask_b32_e32 v50, v192, v50, vcc
	v_cmp_lt_i32_e32 vcc, 31, v139
	v_add_u32_e32 v139, 24, v200
	s_nop 0
	v_cndmask_b32_e32 v34, v192, v34, vcc
	v_cmp_lt_i32_e32 vcc, -1, v139
	s_nop 1
	v_cndmask_b32_e32 v51, v192, v51, vcc
	v_cmp_lt_i32_e32 vcc, 31, v139
	v_add_u32_e32 v139, 19, v200
	s_nop 0
	v_cndmask_b32_e32 v35, v192, v35, vcc
	v_cmp_lt_i32_e32 vcc, -1, v139
	s_nop 1
	v_cndmask_b32_e32 v52, v192, v52, vcc
	v_cmp_lt_i32_e32 vcc, 31, v139
	v_add_u32_e32 v139, 18, v200
	s_nop 0
	v_cndmask_b32_e32 v36, v192, v36, vcc
	v_cmp_lt_i32_e32 vcc, -1, v139
	s_nop 1
	v_cndmask_b32_e32 v53, v192, v53, vcc
	v_cmp_lt_i32_e32 vcc, 31, v139
	v_add_u32_e32 v139, 17, v200
	s_nop 0
	v_cndmask_b32_e32 v37, v192, v37, vcc
	v_cmp_lt_i32_e32 vcc, -1, v139
	s_nop 1
	v_cndmask_b32_e32 v54, v192, v54, vcc
	v_cmp_lt_i32_e32 vcc, 31, v139
	v_add_u32_e32 v139, 16, v200
	s_nop 0
	v_cndmask_b32_e32 v38, v192, v38, vcc
	v_cmp_lt_i32_e32 vcc, -1, v139
	s_nop 1
	v_cndmask_b32_e32 v55, v192, v55, vcc
	v_cmp_lt_i32_e32 vcc, 31, v139
	v_add_u32_e32 v139, 11, v200
	s_nop 0
	v_cndmask_b32_e32 v39, v192, v39, vcc
	v_cmp_lt_i32_e32 vcc, -1, v139
	s_nop 1
	v_cndmask_b32_e32 v56, v192, v56, vcc
	v_cmp_lt_i32_e32 vcc, 31, v139
	v_add_u32_e32 v139, 10, v200
	s_nop 0
	v_cndmask_b32_e32 v40, v192, v40, vcc
	v_cmp_lt_i32_e32 vcc, -1, v139
	s_nop 1
	v_cndmask_b32_e32 v57, v192, v57, vcc
	v_cmp_lt_i32_e32 vcc, 31, v139
	v_add_u32_e32 v139, 9, v200
	s_nop 0
	v_cndmask_b32_e32 v41, v192, v41, vcc
	v_cmp_lt_i32_e32 vcc, -1, v139
	s_nop 1
	v_cndmask_b32_e32 v58, v192, v58, vcc
	v_cmp_lt_i32_e32 vcc, 31, v139
	v_add_u32_e32 v139, 8, v200
	s_nop 0
	v_cndmask_b32_e32 v42, v192, v42, vcc
	v_cmp_lt_i32_e32 vcc, -1, v139
	s_nop 1
	v_cndmask_b32_e32 v59, v192, v59, vcc
	v_cmp_lt_i32_e32 vcc, 31, v139
	v_add_u32_e32 v139, 3, v200
	s_nop 0
	v_cndmask_b32_e32 v43, v192, v43, vcc
	v_cmp_lt_i32_e32 vcc, -1, v139
	s_nop 1
	v_cndmask_b32_e32 v60, v192, v60, vcc
	v_cmp_lt_i32_e32 vcc, 31, v139
	v_add_u32_e32 v139, 2, v200
	s_nop 0
	v_cndmask_b32_e32 v44, v192, v44, vcc
	v_cmp_lt_i32_e32 vcc, -1, v139
	s_nop 1
	v_cndmask_b32_e32 v61, v192, v61, vcc
	v_cmp_lt_i32_e32 vcc, 31, v139
	v_add_u32_e32 v139, 1, v200
	s_nop 0
	v_cndmask_b32_e32 v45, v192, v45, vcc
	v_cmp_lt_i32_e32 vcc, -1, v139
	s_nop 1
	v_cndmask_b32_e32 v62, v192, v62, vcc
	v_cmp_lt_i32_e32 vcc, 31, v139
	s_nop 1
	v_cndmask_b32_e32 v46, v192, v46, vcc
	v_cmp_lt_i32_e32 vcc, -1, v200
	s_nop 1
	v_cndmask_b32_e32 v63, v192, v63, vcc
	v_cmp_lt_i32_e32 vcc, 31, v200
	s_nop 1
	v_cndmask_b32_e32 v47, v192, v47, vcc
.LBB0_3035:
	v_max_f32_e32 v139, v49, v49
	v_max_f32_e32 v160, v48, v48
	v_max_f32_e32 v139, v160, v139
	v_max3_f32 v160, v50, v51, v33
	v_max3_f32 v139, v139, v32, v34
	v_max3_f32 v139, v139, v35, v52
	v_max3_f32 v160, v160, v54, v55
	v_max3_f32 v139, v139, v53, v36
	v_max3_f32 v160, v160, v38, v39
	v_max3_f32 v139, v139, v37, v56
	v_max3_f32 v160, v160, v58, v59
	v_max3_f32 v139, v139, v57, v40
	v_max3_f32 v160, v160, v42, v43
	v_max3_f32 v139, v139, v41, v60
	v_max3_f32 v160, v160, v62, v63
	v_max3_f32 v139, v139, v61, v44
	v_max3_f32 v160, v160, v46, v47
	v_max3_f32 v139, v139, v45, v160
	v_mov_b32_e32 v160, v139
	s_nop 1
	v_permlane32_swap_b32_e32 v139, v160
	v_max_f32_e32 v160, v160, v160
	v_max_f32_e32 v139, v139, v139
	v_max_f32_e32 v139, v139, v160
	v_cmp_lg_f32_e64 s[6:7], s48, v139
	s_xor_b64 s[0:1], s[30:31], -1
	s_and_b64 s[0:1], s[6:7], s[0:1]
	v_cmp_lt_f32_e32 vcc, s16, v139
	s_or_b64 s[54:55], vcc, s[0:1]
	v_cndmask_b32_e64 v160, 0, 1, s[54:55]
	v_cmp_ne_u32_e32 vcc, 0, v160
	s_cbranch_vccz .LBB0_3039
	v_cndmask_b32_e64 v160, 0, v139, s[0:1]
	v_max_f32_e32 v139, v139, v139
	v_max_f32_e32 v139, 0, v139
	v_cndmask_b32_e64 v160, v160, v139, s[30:31]
	v_exp_f32_e64 v139, -v160
	s_nop 0
	v_cndmask_b32_e64 v139, v139, 1.0, s[0:1]
	s_and_saveexec_b64 s[0:1], s[4:5]
	ds_write_b32 v167, v139 offset:49152
	s_or_b64 exec, exec, s[0:1]
	s_waitcnt lgkmcnt(0)
	ds_read_b128 v[202:205], v168 offset:49216
	ds_read_b128 v[206:209], v168 offset:49248
	ds_read_b128 v[210:213], v168 offset:49152
	ds_read_b128 v[214:217], v168 offset:49184
	v_mul_f32_e32 v196, v196, v139
	v_add_f32_e64 v48, v48, -v160
	v_add_f32_e64 v49, v49, -v160
	v_add_f32_e64 v32, v32, -v160
	v_add_f32_e64 v33, v33, -v160
	v_add_f32_e64 v50, v50, -v160
	v_add_f32_e64 v51, v51, -v160
	v_add_f32_e64 v34, v34, -v160
	v_add_f32_e64 v35, v35, -v160
	v_add_f32_e64 v52, v52, -v160
	v_add_f32_e64 v53, v53, -v160
	v_add_f32_e64 v36, v36, -v160
	v_add_f32_e64 v37, v37, -v160
	v_add_f32_e64 v54, v54, -v160
	v_add_f32_e64 v55, v55, -v160
	v_add_f32_e64 v38, v38, -v160
	v_add_f32_e64 v39, v39, -v160
	v_add_f32_e64 v56, v56, -v160
	v_add_f32_e64 v57, v57, -v160
	v_add_f32_e64 v40, v40, -v160
	v_add_f32_e64 v41, v41, -v160
	v_add_f32_e64 v58, v58, -v160
	v_add_f32_e64 v59, v59, -v160
	v_add_f32_e64 v42, v42, -v160
	v_add_f32_e64 v43, v43, -v160
	v_add_f32_e64 v60, v60, -v160
	v_add_f32_e64 v61, v61, -v160
	v_add_f32_e64 v44, v44, -v160
	v_add_f32_e64 v45, v45, -v160
	v_add_f32_e64 v62, v62, -v160
	v_add_f32_e64 v63, v63, -v160
	v_add_f32_e64 v46, v46, -v160
	v_add_f32_e64 v47, v47, -v160
	v_add_f32_e32 v197, v197, v160
	s_or_b64 s[30:31], s[30:31], s[6:7]
	s_waitcnt lgkmcnt(0)
	v_mul_f32_e32 v14, v14, v208
	v_mul_f32_e32 v15, v15, v209
	v_mul_f32_e32 v10, v10, v204
	v_mul_f32_e32 v11, v11, v205
	v_mul_f32_e32 v6, v6, v216
	v_mul_f32_e32 v7, v7, v217
	v_mul_f32_e32 v2, v2, v212
	v_mul_f32_e32 v3, v3, v213
	v_mul_f32_e32 v12, v12, v206
	v_mul_f32_e32 v13, v13, v207
	v_mul_f32_e32 v8, v8, v202
	v_mul_f32_e32 v9, v9, v203
	v_mul_f32_e32 v4, v4, v214
	v_mul_f32_e32 v5, v5, v215
	v_mul_f32_e32 v0, v0, v210
	v_mul_f32_e32 v1, v1, v211
	v_mul_f32_e32 v30, v30, v208
	v_mul_f32_e32 v31, v31, v209
	v_mul_f32_e32 v26, v26, v204
	v_mul_f32_e32 v27, v27, v205
	v_mul_f32_e32 v22, v22, v216
	v_mul_f32_e32 v23, v23, v217
	v_mul_f32_e32 v18, v18, v212
	v_mul_f32_e32 v19, v19, v213
	v_mul_f32_e32 v28, v28, v206
	v_mul_f32_e32 v29, v29, v207
	v_mul_f32_e32 v24, v24, v202
	v_mul_f32_e32 v25, v25, v203
	v_mul_f32_e32 v20, v20, v214
	v_mul_f32_e32 v21, v21, v215
	v_mul_f32_e32 v16, v16, v210
	v_mul_f32_e32 v17, v17, v211
.LBB0_3039:
	v_exp_f32_e32 v203, v48
	v_exp_f32_e32 v202, v32
	v_exp_f32_e32 v49, v49
	v_exp_f32_e32 v48, v33
	v_exp_f32_e32 v205, v50
	v_exp_f32_e32 v204, v34
	v_exp_f32_e32 v51, v51
	v_exp_f32_e32 v50, v35
	v_exp_f32_e32 v209, v52
	v_exp_f32_e32 v53, v53
	v_exp_f32_e32 v211, v54
	v_exp_f32_e32 v55, v55
	v_cvt_pk_bf16_f32 v32, v203, v49
	v_cvt_pk_bf16_f32 v33, v205, v51
	v_cvt_pk_bf16_f32 v34, v209, v53
	v_cvt_pk_bf16_f32 v35, v211, v55
	v_add_f32_e32 v206, 0, v202
	v_add_f32_e32 v207, 0, v203
	v_mfma_f32_32x32x16_bf16 v[0:15], v[32:35], v[100:103], v[0:15]
	v_add_f32_e64 v100, v48, v206
	v_add_f32_e64 v101, v49, v207
	v_exp_f32_e32 v103, v56
	v_exp_f32_e32 v57, v57
	v_exp_f32_e32 v207, v58
	v_exp_f32_e32 v59, v59
	v_exp_f32_e32 v213, v60
	v_exp_f32_e32 v49, v61
	s_waitcnt lgkmcnt(0)
	v_mfma_f32_32x32x16_bf16 v[16:31], v[32:35], v[108:111], v[16:31]
	v_exp_f32_e32 v61, v62
	v_exp_f32_e32 v63, v63
	v_cvt_pk_bf16_f32 v32, v103, v57
	v_cvt_pk_bf16_f32 v33, v207, v59
	v_cvt_pk_bf16_f32 v34, v213, v49
	v_cvt_pk_bf16_f32 v35, v61, v63
	v_exp_f32_e32 v208, v36
	v_mfma_f32_32x32x16_bf16 v[0:15], v[32:35], v[92:95], v[0:15]
	v_exp_f32_e32 v52, v37
	v_add_f32_e32 v100, v204, v100
	v_add_f32_e32 v101, v205, v101
	v_exp_f32_e32 v210, v38
	v_exp_f32_e32 v54, v39
	v_add_f32_e32 v92, v50, v100
	v_add_f32_e32 v93, v51, v101
	v_exp_f32_e32 v102, v40
	v_add_f32_e32 v36, v208, v92
	v_add_f32_e32 v37, v209, v93
	v_mfma_f32_32x32x16_bf16 v[16:31], v[32:35], v[104:107], v[16:31]
	v_cvt_pk_bf16_f32 v32, v202, v48
	v_cvt_pk_bf16_f32 v33, v204, v50
	v_cvt_pk_bf16_f32 v34, v208, v52
	v_cvt_pk_bf16_f32 v35, v210, v54
	v_exp_f32_e32 v56, v41
	v_add_f32_e32 v36, v52, v36
	v_add_f32_e32 v37, v53, v37
	v_exp_f32_e32 v206, v42
	v_mfma_f32_32x32x16_bf16 v[0:15], v[32:35], v[84:87], v[0:15]
	v_add_f32_e64 v36, v210, v36
	v_add_f32_e64 v37, v211, v37
	v_exp_f32_e32 v58, v43
	v_add_f32_e32 v36, v54, v36
	v_add_f32_e32 v37, v55, v37
	v_exp_f32_e32 v212, v44
	v_exp_f32_e32 v48, v45
	v_exp_f32_e32 v60, v46
	v_exp_f32_e32 v62, v47
	v_mfma_f32_32x32x16_bf16 v[16:31], v[32:35], v[96:99], v[16:31]
	v_add_f32_e64 v32, v102, v36
	v_add_f32_e64 v33, v103, v37
	s_andn2_b64 s[0:1], s[34:35], exec
	v_add_f32_e64 v32, v56, v32
	v_add_f32_e64 v33, v57, v33
	s_and_b64 s[6:7], s[30:31], exec
	v_add_f32_e32 v36, v206, v32
	v_add_f32_e32 v37, v207, v33
	v_cvt_pk_bf16_f32 v32, v102, v56
	v_cvt_pk_bf16_f32 v33, v206, v58
	v_cvt_pk_bf16_f32 v34, v212, v48
	v_cvt_pk_bf16_f32 v35, v60, v62
	s_or_b64 s[30:31], s[0:1], s[6:7]
	v_mfma_f32_32x32x16_bf16 v[0:15], v[32:35], v[80:83], v[0:15]
	v_add_f32_e64 v36, v58, v36
	v_add_f32_e64 v37, v59, v37
	v_add_f32_e64 v36, v212, v36
	v_add_f32_e64 v37, v213, v37
	v_add_f32_e64 v36, v48, v36
	v_add_f32_e64 v37, v49, v37
	v_add_f32_e32 v36, v60, v36
	v_add_f32_e32 v37, v61, v37
	v_mfma_f32_32x32x16_bf16 v[16:31], v[32:35], v[88:91], v[16:31]
	v_add_f32_e64 v36, v62, v36
	v_add_f32_e64 v37, v63, v37
	v_add_f32_e32 v36, v36, v37
	v_add_f32_e32 v196, v196, v36
	s_branch .LBB0_3025

.LBB0_3045:
	v_add_u32_e32 v32, s34, v199
	v_cvt_f32_i32_e32 v32, v32
	s_lshl_b32 s6, 1, s39
	v_and_b32_e32 v33, s6, v198
	v_cmp_ne_u32_e32 vcc, 0, v33
	v_fma_f32 v32, v137, v32, -v197
	s_or_b64 vcc, s[0:1], vcc
	v_cndmask_b32_e32 v32, v192, v32, vcc
	v_add_f32_e32 v52, v144, v32
	v_add_f32_e32 v53, v145, v32
	v_add_u32_e32 v144, s36, v165
	ds_read_b128 v[80:83], v144
	ds_read_b128 v[96:99], v144 offset:512
	ds_read_b128 v[100:103], v144 offset:2048
	ds_read_b128 v[104:107], v144 offset:2560
	v_add_f32_e32 v48, v136, v32
	v_add_f32_e32 v49, v137, v32
	v_add_f32_e32 v50, v142, v32
	v_add_f32_e32 v51, v143, v32
	v_add_f32_e32 v54, v146, v32
	v_add_f32_e32 v55, v147, v32
	v_add_f32_e32 v56, v148, v32
	v_add_f32_e32 v57, v149, v32
	v_add_f32_e32 v58, v150, v32
	v_add_f32_e32 v59, v151, v32
	v_add_f32_e32 v60, v152, v32
	v_add_f32_e32 v61, v153, v32
	v_add_f32_e32 v62, v154, v32
	v_add_f32_e32 v63, v155, v32
	v_mov_b32_e32 v139, v138
	v_add_f32_e32 v46, v138, v62
	v_add_f32_e32 v47, v139, v63
	v_add_f32_e32 v44, v138, v60
	v_add_f32_e32 v45, v139, v61
	v_add_f32_e32 v42, v138, v58
	v_add_f32_e32 v43, v139, v59
	v_add_f32_e32 v40, v138, v56
	v_add_f32_e32 v41, v139, v57
	v_add_f32_e32 v38, v138, v54
	v_add_f32_e32 v39, v139, v55
	v_add_f32_e32 v36, v138, v52
	v_add_f32_e32 v37, v139, v53
	v_add_f32_e32 v34, v138, v50
	v_add_f32_e32 v35, v139, v51
	v_add_f32_e32 v32, v140, v48
	v_add_f32_e32 v33, v141, v49
	v_add_u32_e32 v148, s36, v166
	ds_read_b64_tr_b16 v[92:93], v148 offset:24576
	ds_read_b64_tr_b16 v[94:95], v148 offset:25088
	ds_read_b64_tr_b16 v[88:89], v148 offset:25600
	ds_read_b64_tr_b16 v[90:91], v148 offset:26112
	ds_read_b128 v[108:111], v144 offset:4096
	ds_read_b128 v[136:139], v144 offset:4608
	s_waitcnt lgkmcnt(0)
	v_mfma_f32_32x32x16_bf16 v[48:63], v[80:83], v[76:79], v[48:63]
	ds_read_b64_tr_b16 v[84:85], v148 offset:26624
	ds_read_b64_tr_b16 v[86:87], v148 offset:27136
	ds_read_b64_tr_b16 v[80:81], v148 offset:27648
	ds_read_b64_tr_b16 v[82:83], v148 offset:28160
	ds_read_b128 v[140:143], v144 offset:6144
	ds_read_b128 v[144:147], v144 offset:6656
	v_mfma_f32_32x32x16_bf16 v[32:47], v[96:99], v[76:79], v[32:47]
	v_mfma_f32_32x32x16_bf16 v[48:63], v[100:103], v[72:75], v[48:63]
	v_mfma_f32_32x32x16_bf16 v[32:47], v[104:107], v[72:75], v[32:47]
	v_mfma_f32_32x32x16_bf16 v[48:63], v[108:111], v[68:71], v[48:63]
	v_mfma_f32_32x32x16_bf16 v[32:47], v[136:139], v[68:71], v[32:47]
	s_waitcnt lgkmcnt(0)
	v_mfma_f32_32x32x16_bf16 v[48:63], v[140:143], v[64:67], v[48:63]
	ds_read_b64_tr_b16 v[96:97], v148 offset:28672
	ds_read_b64_tr_b16 v[98:99], v148 offset:29184
	ds_read_b64_tr_b16 v[76:77], v148 offset:29696
	ds_read_b64_tr_b16 v[78:79], v148 offset:30208
	v_mfma_f32_32x32x16_bf16 v[32:47], v[144:147], v[64:67], v[32:47]
	ds_read_b64_tr_b16 v[72:73], v148 offset:30720
	ds_read_b64_tr_b16 v[74:75], v148 offset:31232
	ds_read_b64_tr_b16 v[68:69], v148 offset:31744
	ds_read_b64_tr_b16 v[70:71], v148 offset:32256
	s_or_b32 s6, s34, 63
	s_cmp_gt_u32 s6, s8
	s_cselect_b64 s[6:7], -1, 0
	s_and_b64 s[0:1], s[0:1], s[6:7]
	s_andn2_b64 vcc, exec, s[0:1]
	s_cbranch_vccnz .LBB0_3047
	v_add_u32_e32 v64, s34, v164
	v_sub_u32_e32 v65, v195, v64
	v_cmp_lt_i32_e32 vcc, -1, v65
	v_xad_u32 v66, v64, -1, v195
	s_nop 0
	v_cndmask_b32_e32 v48, v192, v48, vcc
	v_cmp_lt_i32_e32 vcc, 31, v65
	s_nop 1
	v_cndmask_b32_e32 v32, v192, v32, vcc
	v_cmp_lt_i32_e32 vcc, -1, v66
	s_nop 1
	v_cndmask_b32_e32 v49, v192, v49, vcc
	v_cmp_lt_i32_e32 vcc, 31, v66
	v_or_b32_e32 v66, 2, v64
	v_sub_u32_e32 v66, v195, v66
	v_cndmask_b32_e32 v33, v192, v33, vcc
	v_cmp_lt_i32_e32 vcc, -1, v66
	v_or_b32_e32 v64, 3, v64
	v_sub_u32_e32 v64, v195, v64
	v_cndmask_b32_e32 v50, v192, v50, vcc
	v_cmp_lt_i32_e32 vcc, 31, v66
	s_nop 1
	v_cndmask_b32_e32 v34, v192, v34, vcc
	v_cmp_lt_i32_e32 vcc, -1, v64
	s_nop 1
	v_cndmask_b32_e32 v51, v192, v51, vcc
	v_cmp_lt_i32_e32 vcc, 31, v64
	v_add_u32_e32 v64, -8, v65
	s_nop 0
	v_cndmask_b32_e32 v35, v192, v35, vcc
	v_cmp_lt_i32_e32 vcc, -1, v64
	s_nop 1
	v_cndmask_b32_e32 v52, v192, v52, vcc
	v_cmp_lt_i32_e32 vcc, 31, v64
	v_add_u32_e32 v64, -9, v65
	s_nop 0
	v_cndmask_b32_e32 v36, v192, v36, vcc
	v_cmp_lt_i32_e32 vcc, -1, v64
	s_nop 1
	v_cndmask_b32_e32 v53, v192, v53, vcc
	v_cmp_lt_i32_e32 vcc, 31, v64
	v_add_u32_e32 v64, -10, v65
	s_nop 0
	v_cndmask_b32_e32 v37, v192, v37, vcc
	v_cmp_lt_i32_e32 vcc, -1, v64
	s_nop 1
	v_cndmask_b32_e32 v54, v192, v54, vcc
	v_cmp_lt_i32_e32 vcc, 31, v64
	v_add_u32_e32 v64, -11, v65
	s_nop 0
	v_cndmask_b32_e32 v38, v192, v38, vcc
	v_cmp_lt_i32_e32 vcc, -1, v64
	s_nop 1
	v_cndmask_b32_e32 v55, v192, v55, vcc
	v_cmp_lt_i32_e32 vcc, 31, v64
	v_add_u32_e32 v64, -16, v65
	s_nop 0
	v_cndmask_b32_e32 v39, v192, v39, vcc
	v_cmp_lt_i32_e32 vcc, -1, v64
	s_nop 1
	v_cndmask_b32_e32 v56, v192, v56, vcc
	v_cmp_lt_i32_e32 vcc, 31, v64
	v_subrev_u32_e32 v64, 17, v65
	s_nop 0
	v_cndmask_b32_e32 v40, v192, v40, vcc
	v_cmp_lt_i32_e32 vcc, -1, v64
	s_nop 1
	v_cndmask_b32_e32 v57, v192, v57, vcc
	v_cmp_lt_i32_e32 vcc, 31, v64
	v_subrev_u32_e32 v64, 18, v65
	s_nop 0
	v_cndmask_b32_e32 v41, v192, v41, vcc
	v_cmp_lt_i32_e32 vcc, -1, v64
	s_nop 1
	v_cndmask_b32_e32 v58, v192, v58, vcc
	v_cmp_lt_i32_e32 vcc, 31, v64
	v_subrev_u32_e32 v64, 19, v65
	s_nop 0
	v_cndmask_b32_e32 v42, v192, v42, vcc
	v_cmp_lt_i32_e32 vcc, -1, v64
	s_nop 1
	v_cndmask_b32_e32 v59, v192, v59, vcc
	v_cmp_lt_i32_e32 vcc, 31, v64
	v_subrev_u32_e32 v64, 24, v65
	s_nop 0
	v_cndmask_b32_e32 v43, v192, v43, vcc
	v_cmp_lt_i32_e32 vcc, -1, v64
	s_nop 1
	v_cndmask_b32_e32 v60, v192, v60, vcc
	v_cmp_lt_i32_e32 vcc, 31, v64
	v_subrev_u32_e32 v64, 25, v65
	s_nop 0
	v_cndmask_b32_e32 v44, v192, v44, vcc
	v_cmp_lt_i32_e32 vcc, -1, v64
	s_nop 1
	v_cndmask_b32_e32 v61, v192, v61, vcc
	v_cmp_lt_i32_e32 vcc, 31, v64
	v_subrev_u32_e32 v64, 26, v65
	s_nop 0
	v_cndmask_b32_e32 v45, v192, v45, vcc
	v_cmp_lt_i32_e32 vcc, -1, v64
	s_nop 1
	v_cndmask_b32_e32 v62, v192, v62, vcc
	v_cmp_lt_i32_e32 vcc, 31, v64
	v_subrev_u32_e32 v64, 27, v65
	s_nop 0
	v_cndmask_b32_e32 v46, v192, v46, vcc
	v_cmp_lt_i32_e32 vcc, -1, v64
	s_nop 1
	v_cndmask_b32_e32 v63, v192, v63, vcc
	v_cmp_lt_i32_e32 vcc, 31, v64
	s_nop 1
	v_cndmask_b32_e32 v47, v192, v47, vcc
.LBB0_3047:
	v_max_f32_e32 v64, v49, v49
	v_max_f32_e32 v65, v48, v48
	v_max_f32_e32 v64, v65, v64
	v_max3_f32 v65, v50, v51, v33
	v_max3_f32 v64, v64, v32, v34
	v_max3_f32 v64, v64, v35, v52
	v_max3_f32 v65, v65, v54, v55
	v_max3_f32 v64, v64, v53, v36
	v_max3_f32 v65, v65, v38, v39
	v_max3_f32 v64, v64, v37, v56
	v_max3_f32 v65, v65, v58, v59
	v_max3_f32 v64, v64, v57, v40
	v_max3_f32 v65, v65, v42, v43
	v_max3_f32 v64, v64, v41, v60
	v_max3_f32 v65, v65, v62, v63
	v_max3_f32 v64, v64, v61, v44
	v_max3_f32 v65, v65, v46, v47
	v_max3_f32 v64, v64, v45, v65
	v_mov_b32_e32 v65, v64
	s_nop 1
	v_permlane32_swap_b32_e32 v64, v65
	v_max_f32_e32 v65, v65, v65
	v_max_f32_e32 v64, v64, v64
	v_max_f32_e32 v64, v64, v65
	v_cmp_lg_f32_e32 vcc, s48, v64
	s_xor_b64 s[0:1], s[30:31], -1
	s_and_b64 s[0:1], vcc, s[0:1]
	v_cmp_lt_f32_e32 vcc, s16, v64
	s_or_b64 s[6:7], vcc, s[0:1]
	v_cndmask_b32_e64 v65, 0, 1, s[6:7]
	v_cmp_ne_u32_e32 vcc, 0, v65
	s_cbranch_vccz .LBB0_3051
	v_cndmask_b32_e64 v65, 0, v64, s[0:1]
	v_max_f32_e32 v64, v64, v64
	v_max_f32_e32 v64, 0, v64
	v_cndmask_b32_e64 v64, v65, v64, s[30:31]
	v_exp_f32_e64 v65, -v64
	s_nop 0
	v_cndmask_b32_e64 v65, v65, 1.0, s[0:1]
	s_and_saveexec_b64 s[0:1], s[4:5]
	ds_write_b32 v167, v65 offset:49152
	s_or_b64 exec, exec, s[0:1]
	s_waitcnt lgkmcnt(0)
	ds_read_b128 v[100:103], v168 offset:49216
	ds_read_b128 v[104:107], v168 offset:49248
	ds_read_b128 v[108:111], v168 offset:49152
	ds_read_b128 v[136:139], v168 offset:49184
	v_mul_f32_e32 v196, v196, v65
	v_add_f32_e64 v48, v48, -v64
	v_add_f32_e64 v49, v49, -v64
	v_add_f32_e64 v32, v32, -v64
	v_add_f32_e64 v33, v33, -v64
	v_add_f32_e64 v50, v50, -v64
	v_add_f32_e64 v51, v51, -v64
	v_add_f32_e64 v34, v34, -v64
	v_add_f32_e64 v35, v35, -v64
	v_add_f32_e64 v52, v52, -v64
	v_add_f32_e64 v53, v53, -v64
	v_add_f32_e64 v36, v36, -v64
	v_add_f32_e64 v37, v37, -v64
	v_add_f32_e64 v54, v54, -v64
	v_add_f32_e64 v55, v55, -v64
	v_add_f32_e64 v38, v38, -v64
	v_add_f32_e64 v39, v39, -v64
	v_add_f32_e64 v56, v56, -v64
	v_add_f32_e64 v57, v57, -v64
	v_add_f32_e64 v40, v40, -v64
	v_add_f32_e64 v41, v41, -v64
	v_add_f32_e64 v58, v58, -v64
	v_add_f32_e64 v59, v59, -v64
	v_add_f32_e64 v42, v42, -v64
	v_add_f32_e64 v43, v43, -v64
	v_add_f32_e64 v60, v60, -v64
	v_add_f32_e64 v61, v61, -v64
	v_add_f32_e64 v44, v44, -v64
	v_add_f32_e64 v45, v45, -v64
	v_add_f32_e64 v62, v62, -v64
	v_add_f32_e64 v63, v63, -v64
	v_add_f32_e64 v46, v46, -v64
	v_add_f32_e64 v47, v47, -v64
	s_waitcnt lgkmcnt(0)
	v_mul_f32_e32 v14, v14, v106
	v_mul_f32_e32 v15, v15, v107
	v_mul_f32_e32 v10, v10, v102
	v_mul_f32_e32 v11, v11, v103
	v_mul_f32_e32 v6, v6, v138
	v_mul_f32_e32 v7, v7, v139
	v_mul_f32_e32 v2, v2, v110
	v_mul_f32_e32 v3, v3, v111
	v_mul_f32_e32 v12, v12, v104
	v_mul_f32_e32 v13, v13, v105
	v_mul_f32_e32 v8, v8, v100
	v_mul_f32_e32 v9, v9, v101
	v_mul_f32_e32 v4, v4, v136
	v_mul_f32_e32 v5, v5, v137
	v_mul_f32_e32 v0, v0, v108
	v_mul_f32_e32 v1, v1, v109
	v_mul_f32_e32 v30, v30, v106
	v_mul_f32_e32 v31, v31, v107
	v_mul_f32_e32 v26, v26, v102
	v_mul_f32_e32 v27, v27, v103
	v_mul_f32_e32 v22, v22, v138
	v_mul_f32_e32 v23, v23, v139
	v_mul_f32_e32 v18, v18, v110
	v_mul_f32_e32 v19, v19, v111
	v_mul_f32_e32 v28, v28, v104
	v_mul_f32_e32 v29, v29, v105
	v_mul_f32_e32 v24, v24, v100
	v_mul_f32_e32 v25, v25, v101
	v_mul_f32_e32 v20, v20, v136
	v_mul_f32_e32 v21, v21, v137
	v_mul_f32_e32 v16, v16, v108
	v_mul_f32_e32 v17, v17, v109
.LBB0_3051:
	v_exp_f32_e32 v65, v48
	v_exp_f32_e32 v64, v32
	v_exp_f32_e32 v49, v49
	v_exp_f32_e32 v48, v33
	v_exp_f32_e32 v67, v50
	v_exp_f32_e32 v66, v34
	v_exp_f32_e32 v51, v51
	v_exp_f32_e32 v50, v35
	v_exp_f32_e32 v103, v52
	v_exp_f32_e32 v53, v53
	v_exp_f32_e32 v105, v54
	v_exp_f32_e32 v55, v55
	v_cvt_pk_bf16_f32 v32, v65, v49
	v_cvt_pk_bf16_f32 v33, v67, v51
	v_cvt_pk_bf16_f32 v34, v103, v53
	v_cvt_pk_bf16_f32 v35, v105, v55
	v_add_f32_e32 v100, 0, v64
	v_add_f32_e32 v101, 0, v65
	v_mfma_f32_32x32x16_bf16 v[0:15], v[32:35], v[92:95], v[0:15]
	v_add_f32_e64 v92, v48, v100
	v_add_f32_e64 v93, v49, v101
	v_exp_f32_e32 v95, v56
	v_exp_f32_e32 v57, v57
	v_exp_f32_e32 v101, v58
	v_exp_f32_e32 v59, v59
	v_exp_f32_e32 v107, v60
	v_exp_f32_e32 v49, v61
	s_waitcnt lgkmcnt(0)
	v_mfma_f32_32x32x16_bf16 v[16:31], v[32:35], v[96:99], v[16:31]
	v_exp_f32_e32 v61, v62
	v_exp_f32_e32 v63, v63
	v_cvt_pk_bf16_f32 v32, v95, v57
	v_cvt_pk_bf16_f32 v33, v101, v59
	v_cvt_pk_bf16_f32 v34, v107, v49
	v_cvt_pk_bf16_f32 v35, v61, v63
	v_exp_f32_e32 v102, v36
	v_mfma_f32_32x32x16_bf16 v[0:15], v[32:35], v[88:91], v[0:15]
	v_exp_f32_e32 v52, v37
	v_add_f32_e32 v92, v66, v92
	v_add_f32_e32 v93, v67, v93
	v_exp_f32_e32 v104, v38
	v_exp_f32_e32 v54, v39
	v_add_f32_e32 v88, v50, v92
	v_add_f32_e32 v89, v51, v93
	v_exp_f32_e32 v94, v40
	v_add_f32_e32 v36, v102, v88
	v_add_f32_e32 v37, v103, v89
	v_mfma_f32_32x32x16_bf16 v[16:31], v[32:35], v[76:79], v[16:31]
	v_cvt_pk_bf16_f32 v32, v64, v48
	v_cvt_pk_bf16_f32 v33, v66, v50
	v_cvt_pk_bf16_f32 v34, v102, v52
	v_cvt_pk_bf16_f32 v35, v104, v54
	v_exp_f32_e32 v56, v41
	v_add_f32_e32 v36, v52, v36
	v_add_f32_e32 v37, v53, v37
	v_exp_f32_e32 v100, v42
	v_mfma_f32_32x32x16_bf16 v[0:15], v[32:35], v[84:87], v[0:15]
	v_add_f32_e64 v36, v104, v36
	v_add_f32_e64 v37, v105, v37
	v_exp_f32_e32 v58, v43
	v_add_f32_e32 v36, v54, v36
	v_add_f32_e32 v37, v55, v37
	v_exp_f32_e32 v106, v44
	v_exp_f32_e32 v48, v45
	v_exp_f32_e32 v60, v46
	v_exp_f32_e32 v62, v47
	v_mfma_f32_32x32x16_bf16 v[16:31], v[32:35], v[72:75], v[16:31]
	v_add_f32_e64 v32, v94, v36
	v_add_f32_e64 v33, v95, v37
	v_add_f32_e64 v32, v56, v32
	v_add_f32_e64 v33, v57, v33
	v_add_f32_e64 v36, v100, v32
	v_add_f32_e64 v37, v101, v33
	v_cvt_pk_bf16_f32 v32, v94, v56
	v_cvt_pk_bf16_f32 v33, v100, v58
	v_cvt_pk_bf16_f32 v34, v106, v48
	v_cvt_pk_bf16_f32 v35, v60, v62
	s_nop 0
	v_mfma_f32_32x32x16_bf16 v[0:15], v[32:35], v[80:83], v[0:15]
	v_add_f32_e64 v36, v58, v36
	v_add_f32_e64 v37, v59, v37
	v_add_f32_e64 v36, v106, v36
	v_add_f32_e64 v37, v107, v37
	v_add_f32_e64 v36, v48, v36
	v_add_f32_e64 v37, v49, v37
	v_add_f32_e32 v36, v60, v36
	v_add_f32_e32 v37, v61, v37
	v_mfma_f32_32x32x16_bf16 v[16:31], v[32:35], v[68:71], v[16:31]
	v_add_f32_e64 v36, v62, v36
	v_add_f32_e64 v37, v63, v37
	v_add_f32_e32 v36, v36, v37
	v_add_f32_e32 v196, v196, v36
